# in-proj GEMM: halves keep their barrier offset across unit boundaries (epilogue of one half overlaps the other half's MFMA segment); first K iteration peeled in 4 GEMM loops so the first MFMA takes C=
# baseline (speedup 1.0000x reference)
; #define PG8_STAGE_B(b, h, bp) PG8_STAGE2(PG8_SB(b, h), (bp) + (h) * hstepB, voffB[0], voffB[1])
; #define PG8_STAGE_A(b, h, ap, NX) do { if constexpr (GATHER) { const unsigned _o0 = (NX) ? vn[h][0] : vc[h][0], _o1 = (NX) ? vn[h][1] : vc[h][1]; PG8_STAGE2(PG8_SA(b, h), (ap), _o0, _o1); } \
;         else { PG8_STAGE2(PG8_SA(b, h), (ap) + (h) * hstepA, voffA[0], voffA[1]); } } while (0)
; #define PG8_LDA(dst, b, h) do { _Pragma("unroll") for (int m = 0; m < 4; ++m) _Pragma("unroll") for (int k = 0; k < 2; ++k) dst[m][k] = *(const LAS bf16x8*)(lds + PG8_SA(b, h) + aoff + m * 2048 + k * 1024); } while (0)
; #define PG8_LDB(dst, b, h) do { _Pragma("unroll") for (int n = 0; n < 2; ++n) _Pragma("unroll") for (int k = 0; k < 2; ++k) dst[n][k] = *(const LAS bf16x8*)(lds + PG8_SB(b, h) + boff + n * 2048 + k * 1024); } while (0)
; #define PG8_MMA(ai, bj, At, Bt) do { __builtin_amdgcn_s_setprio(1); _Pragma("unroll") for (int m = 0; m < 4; ++m) _Pragma("unroll") for (int n = 0; n < 2; ++n) _Pragma("unroll") for (int k = 0; k < 2; ++k) \
;         acc[ai][bj][m][n] = __builtin_amdgcn_mfma_f32_16x16x32_bf16(Bt[n][k], At[m][k], acc[ai][bj][m][n], 0, 0, 0); __builtin_amdgcn_s_setprio(0); } while (0)
; #define PG8_WAIT_V(n) asm volatile("s_waitcnt vmcnt(" #n ")" ::: "memory")
; #define PG8_BAR __builtin_amdgcn_s_barrier()
; template <class Epi, class Sched, bool GATHER, bool LIGHTSKIP = false>
; __device__ __forceinline__ void gemm_phase(LAS unsigned char* lds, LAS unsigned char* xl, const int lda, const int ldb, const int K, const Sched& S, const Epi& E) {
;     ...
;             PG8_LDB(B0, 0, 0); PG8_LDB(B1, 0, 1); PG8_SCHED; PG8_LDA(At, 0, 0); PG8_STAGE_A(1, 1, a1, false);
;             PG8_WAIT_V(8); PG8_WAIT_L(0); PG8_BAR; PG8_MMA(0, 0, At, B0); PG8_MMA(0, 1, At, B1); PG8_BAR; PG8_SCHED;
;             PG8_LDA(At, 0, 1); PG8_STAGE_B(0, 0, b2); PG8_STAGE_B(0, 1, b2); PG8_STAGE_A(0, 0, a2, last);
;             PG8_WAIT_V(8); PG8_WAIT_L(0); PG8_BAR; if (!light) { PG8_MMA(1, 0, At, B0); PG8_MMA(1, 1, At, B1); } PG8_BAR; PG8_SCHED;
;     ...
; #pragma unroll
;         for (int a = 0; a < 2; ++a)
; #pragma unroll
;             for (int b = 0; b < 2; ++b)
; #pragma unroll
;                 for (int m = 0; m < 4; ++m)
; #pragma unroll
;                     for (int n = 0; n < 2; ++n) acc[a][b][m][n] = (f32x4){0.f, 0.f, 0.f, 0.f};
;         cur = nxt; cA = nA; cB = nB; ++ui;
.LBB0_152:
	s_add_u32 s22, s22, 0x80080
	s_addc_u32 s23, s23, 0
	s_add_u32 s45, s28, 0x100
	s_addc_u32 s46, s29, 0
	s_mov_b32 s47, -2
	ds_read_b128 v[152:155], v148
	ds_read_b128 v[156:159], v148 offset:1024
	ds_read_b128 v[160:163], v148 offset:2048
	ds_read_b128 v[164:167], v148 offset:3072
	ds_read_b128 v[168:171], v149
	ds_read_b128 v[172:175], v149 offset:1024
	ds_read_b128 v[176:179], v149 offset:2048
	ds_read_b128 v[180:183], v149 offset:3072
	s_add_u32 s28, s22, 0xfff80080
	s_addc_u32 s29, s23, -1
	s_cmp_eq_u32 s47, 28
	s_cselect_b32 s31, s19, s29
	s_cselect_b32 s30, s18, s28
	s_cselect_b32 s29, s21, s46
	s_cselect_b32 s28, s20, s45
	v_lshl_add_u64 v[216:217], s[22:23], 0, v[138:139]
	s_add_i32 m0, s7, 0xc000
	ds_read_b128 v[184:187], v150
	ds_read_b128 v[188:191], v150 offset:1024
	ds_read_b128 v[192:195], v150 offset:2048
	ds_read_b128 v[196:199], v150 offset:3072
	ds_read_b128 v[200:203], v150 offset:4096
	ds_read_b128 v[204:207], v150 offset:5120
	ds_read_b128 v[208:211], v150 offset:6144
	ds_read_b128 v[212:215], v150 offset:7168
	global_load_lds_dwordx4 v[216:217], off
	v_lshl_add_u64 v[216:217], s[22:23], 0, v[140:141]
	s_add_i32 m0, s7, 0xe000
	s_nop 0
	global_load_lds_dwordx4 v[216:217], off
	s_waitcnt vmcnt(8)
	s_waitcnt lgkmcnt(0)
	s_barrier
	s_waitcnt lgkmcnt(0)
	v_mfma_f32_16x16x32_bf16 v[126:129], v[152:155], v[184:187], 0
	v_mfma_f32_16x16x32_bf16 v[122:125], v[160:163], v[184:187], 0
	v_mfma_f32_16x16x32_bf16 v[118:121], v[152:155], v[192:195], 0
	v_mfma_f32_16x16x32_bf16 v[114:117], v[160:163], v[192:195], 0
	v_mfma_f32_16x16x32_bf16 v[102:105], v[152:155], v[200:203], 0
	v_mfma_f32_16x16x32_bf16 v[98:101], v[160:163], v[200:203], 0
	v_mfma_f32_16x16x32_bf16 v[86:89], v[152:155], v[208:211], 0
	v_mfma_f32_16x16x32_bf16 v[82:85], v[160:163], v[208:211], 0
	v_mfma_f32_16x16x32_bf16 v[126:129], v[156:159], v[188:191], v[126:129]
	v_mfma_f32_16x16x32_bf16 v[122:125], v[164:167], v[188:191], v[122:125]
	v_mfma_f32_16x16x32_bf16 v[118:121], v[156:159], v[196:199], v[118:121]
	v_mfma_f32_16x16x32_bf16 v[114:117], v[164:167], v[196:199], v[114:117]
	v_mfma_f32_16x16x32_bf16 v[102:105], v[156:159], v[204:207], v[102:105]
	v_mfma_f32_16x16x32_bf16 v[98:101], v[164:167], v[204:207], v[98:101]
	v_mfma_f32_16x16x32_bf16 v[86:89], v[156:159], v[212:215], v[86:89]
	v_mfma_f32_16x16x32_bf16 v[82:85], v[164:167], v[212:215], v[82:85]
	v_mfma_f32_16x16x32_bf16 v[110:113], v[168:171], v[184:187], 0
	v_mfma_f32_16x16x32_bf16 v[106:109], v[176:179], v[184:187], 0
	v_mfma_f32_16x16x32_bf16 v[94:97], v[168:171], v[192:195], 0
	v_mfma_f32_16x16x32_bf16 v[90:93], v[176:179], v[192:195], 0
	v_mfma_f32_16x16x32_bf16 v[78:81], v[168:171], v[200:203], 0
	v_mfma_f32_16x16x32_bf16 v[74:77], v[176:179], v[200:203], 0
	v_mfma_f32_16x16x32_bf16 v[70:73], v[168:171], v[208:211], 0
	v_mfma_f32_16x16x32_bf16 v[66:69], v[176:179], v[208:211], 0
	v_mfma_f32_16x16x32_bf16 v[110:113], v[172:175], v[188:191], v[110:113]
	v_mfma_f32_16x16x32_bf16 v[106:109], v[180:183], v[188:191], v[106:109]
	v_mfma_f32_16x16x32_bf16 v[94:97], v[172:175], v[196:199], v[94:97]
	v_mfma_f32_16x16x32_bf16 v[90:93], v[180:183], v[196:199], v[90:93]
	v_mfma_f32_16x16x32_bf16 v[78:81], v[172:175], v[204:207], v[78:81]
	v_mfma_f32_16x16x32_bf16 v[74:77], v[180:183], v[204:207], v[74:77]
	v_mfma_f32_16x16x32_bf16 v[70:73], v[172:175], v[212:215], v[70:73]
	v_mfma_f32_16x16x32_bf16 v[66:69], v[180:183], v[212:215], v[66:69]
	s_barrier
	s_add_i32 s48, s38, s4
	v_lshl_add_u64 v[216:217], s[28:29], 0, v[134:135]
	s_mov_b32 m0, s48
	ds_read_b128 v[184:187], v150 offset:16384
	ds_read_b128 v[188:191], v150 offset:17408
	ds_read_b128 v[192:195], v150 offset:18432
	ds_read_b128 v[196:199], v150 offset:19456
	ds_read_b128 v[200:203], v150 offset:20480
	ds_read_b128 v[204:207], v150 offset:21504
	ds_read_b128 v[208:211], v150 offset:22528
	ds_read_b128 v[212:215], v150 offset:23552
	global_load_lds_dwordx4 v[216:217], off
	s_add_i32 m0, s48, 0x2000
	s_add_u32 s48, s28, 0x80000
	v_lshl_add_u64 v[218:219], s[28:29], 0, v[130:131]
	s_addc_u32 s49, s29, 0
	s_add_i32 s50, s39, s4
	global_load_lds_dwordx4 v[218:219], off
	v_lshl_add_u64 v[220:221], s[48:49], 0, v[134:135]
	s_mov_b32 m0, s50
	v_lshl_add_u64 v[222:223], s[30:31], 0, v[132:133]
	global_load_lds_dwordx4 v[220:221], off
	v_lshl_add_u64 v[220:221], s[48:49], 0, v[130:131]
	s_add_i32 m0, s50, 0x2000
	s_nop 0
	global_load_lds_dwordx4 v[220:221], off
	v_lshl_add_u64 v[220:221], s[30:31], 0, v[136:137]
	s_mov_b32 m0, s7
	s_nop 0
	global_load_lds_dwordx4 v[220:221], off
	s_mov_b32 m0, s26
	s_nop 0
	global_load_lds_dwordx4 v[222:223], off
	s_waitcnt vmcnt(8)
	s_waitcnt lgkmcnt(0)
	s_barrier
; #define PG8_STAGE_B(b, h, bp) PG8_STAGE2(PG8_SB(b, h), (bp) + (h) * hstepB, voffB[0], voffB[1])
; #define PG8_STAGE_A(b, h, ap, NX) do { if constexpr (GATHER) { const unsigned _o0 = (NX) ? vn[h][0] : vc[h][0], _o1 = (NX) ? vn[h][1] : vc[h][1]; PG8_STAGE2(PG8_SA(b, h), (ap), _o0, _o1); } \
;         else { PG8_STAGE2(PG8_SA(b, h), (ap) + (h) * hstepA, voffA[0], voffA[1]); } } while (0)
; #define PG8_LDA(dst, b, h) do { _Pragma("unroll") for (int m = 0; m < 4; ++m) _Pragma("unroll") for (int k = 0; k < 2; ++k) dst[m][k] = *(const LAS bf16x8*)(lds + PG8_SA(b, h) + aoff + m * 2048 + k * 1024); } while (0)
; #define PG8_LDB(dst, b, h) do { _Pragma("unroll") for (int n = 0; n < 2; ++n) _Pragma("unroll") for (int k = 0; k < 2; ++k) dst[n][k] = *(const LAS bf16x8*)(lds + PG8_SB(b, h) + boff + n * 2048 + k * 1024); } while (0)
; #define PG8_MMA(ai, bj, At, Bt) do { __builtin_amdgcn_s_setprio(1); _Pragma("unroll") for (int m = 0; m < 4; ++m) _Pragma("unroll") for (int n = 0; n < 2; ++n) _Pragma("unroll") for (int k = 0; k < 2; ++k) \
;         acc[ai][bj][m][n] = __builtin_amdgcn_mfma_f32_16x16x32_bf16(Bt[n][k], At[m][k], acc[ai][bj][m][n], 0, 0, 0); __builtin_amdgcn_s_setprio(0); } while (0)
; #define PG8_WAIT_V(n) asm volatile("s_waitcnt vmcnt(" #n ")" ::: "memory")
; #define PG8_WAIT_L(n) asm volatile("s_waitcnt lgkmcnt(" #n ")" ::: "memory")
; #define PG8_BAR __builtin_amdgcn_s_barrier()
; #define PG8_SCHED __builtin_amdgcn_sched_barrier(0)
; template <class Epi, class Sched, bool GATHER, bool LIGHTSKIP = false>
; __device__ __forceinline__ void gemm_phase(LAS unsigned char* lds, LAS unsigned char* xl, const int lda, const int ldb, const int K, const Sched& S, const Epi& E) {
;     ...
;             PG8_WAIT_V(8); PG8_WAIT_L(0); PG8_BAR; PG8_MMA(0, 0, At, B0); PG8_MMA(0, 1, At, B1); PG8_BAR; PG8_SCHED;
;             PG8_LDA(At, 0, 1); PG8_STAGE_B(0, 0, b2); PG8_STAGE_B(0, 1, b2); PG8_STAGE_A(0, 0, a2, last);
;             PG8_WAIT_V(8); PG8_WAIT_L(0); PG8_BAR; if (!light) { PG8_MMA(1, 0, At, B0); PG8_MMA(1, 1, At, B1); } PG8_BAR; PG8_SCHED;
;             PG8_LDB(B0, 1, 0); PG8_LDB(B1, 1, 1); PG8_SCHED; PG8_LDA(At, 1, 0); PG8_STAGE_A(0, 1, a2, last);
;             PG8_WAIT_V(8); PG8_WAIT_L(0); PG8_BAR; PG8_MMA(0, 0, At, B0); PG8_MMA(0, 1, At, B1); PG8_BAR; PG8_SCHED;
	s_waitcnt lgkmcnt(0)
	v_mfma_f32_16x16x32_bf16 v[62:65], v[152:155], v[184:187], 0
	v_mfma_f32_16x16x32_bf16 v[58:61], v[160:163], v[184:187], 0
	v_mfma_f32_16x16x32_bf16 v[54:57], v[152:155], v[192:195], 0
	v_mfma_f32_16x16x32_bf16 v[50:53], v[160:163], v[192:195], 0
	v_mfma_f32_16x16x32_bf16 v[38:41], v[152:155], v[200:203], 0
	v_mfma_f32_16x16x32_bf16 v[34:37], v[160:163], v[200:203], 0
	v_mfma_f32_16x16x32_bf16 v[22:25], v[152:155], v[208:211], 0
	v_mfma_f32_16x16x32_bf16 v[18:21], v[160:163], v[208:211], 0
	v_mfma_f32_16x16x32_bf16 v[62:65], v[156:159], v[188:191], v[62:65]
	v_mfma_f32_16x16x32_bf16 v[58:61], v[164:167], v[188:191], v[58:61]
	v_mfma_f32_16x16x32_bf16 v[54:57], v[156:159], v[196:199], v[54:57]
	v_mfma_f32_16x16x32_bf16 v[50:53], v[164:167], v[196:199], v[50:53]
	v_mfma_f32_16x16x32_bf16 v[38:41], v[156:159], v[204:207], v[38:41]
	v_mfma_f32_16x16x32_bf16 v[34:37], v[164:167], v[204:207], v[34:37]
	v_mfma_f32_16x16x32_bf16 v[22:25], v[156:159], v[212:215], v[22:25]
	v_mfma_f32_16x16x32_bf16 v[18:21], v[164:167], v[212:215], v[18:21]
	v_mfma_f32_16x16x32_bf16 v[46:49], v[168:171], v[184:187], 0
	v_mfma_f32_16x16x32_bf16 v[42:45], v[176:179], v[184:187], 0
	v_mfma_f32_16x16x32_bf16 v[30:33], v[168:171], v[192:195], 0
	v_mfma_f32_16x16x32_bf16 v[26:29], v[176:179], v[192:195], 0
	v_mfma_f32_16x16x32_bf16 v[14:17], v[168:171], v[200:203], 0
	v_mfma_f32_16x16x32_bf16 v[10:13], v[176:179], v[200:203], 0
	v_mfma_f32_16x16x32_bf16 v[6:9], v[168:171], v[208:211], 0
	v_mfma_f32_16x16x32_bf16 v[2:5], v[176:179], v[208:211], 0
	v_mfma_f32_16x16x32_bf16 v[46:49], v[172:175], v[188:191], v[46:49]
	v_mfma_f32_16x16x32_bf16 v[42:45], v[180:183], v[188:191], v[42:45]
	v_mfma_f32_16x16x32_bf16 v[30:33], v[172:175], v[196:199], v[30:33]
	v_mfma_f32_16x16x32_bf16 v[26:29], v[180:183], v[196:199], v[26:29]
	v_mfma_f32_16x16x32_bf16 v[14:17], v[172:175], v[204:207], v[14:17]
	v_mfma_f32_16x16x32_bf16 v[10:13], v[180:183], v[204:207], v[10:13]
	v_mfma_f32_16x16x32_bf16 v[6:9], v[172:175], v[212:215], v[6:9]
	v_mfma_f32_16x16x32_bf16 v[2:5], v[180:183], v[212:215], v[2:5]
	s_barrier
	s_add_i32 s48, 0, 0x18000
	v_add_u32_e32 v151, s48, v146
	s_add_i32 s49, 0, 0x1c000
	ds_read_b128 v[152:155], v151
	ds_read_b128 v[156:159], v151 offset:1024
	ds_read_b128 v[160:163], v151 offset:2048
	ds_read_b128 v[164:167], v151 offset:3072
	v_add_u32_e32 v151, s49, v146
	ds_read_b128 v[168:171], v151
	ds_read_b128 v[172:175], v151 offset:1024
	ds_read_b128 v[176:179], v151 offset:2048
	ds_read_b128 v[180:183], v151 offset:3072
	s_add_u32 s30, s30, 0x80000
	s_addc_u32 s31, s31, 0
	s_mov_b32 m0, s27
	v_lshl_add_u64 v[224:225], s[30:31], 0, v[136:137]
	ds_read_b128 v[184:187], v150 offset:32768
	ds_read_b128 v[188:191], v150 offset:33792
	ds_read_b128 v[192:195], v150 offset:34816
	ds_read_b128 v[196:199], v150 offset:35840
	ds_read_b128 v[200:203], v150 offset:36864
	ds_read_b128 v[204:207], v150 offset:37888
	ds_read_b128 v[208:211], v150 offset:38912
	ds_read_b128 v[212:215], v150 offset:39936
	global_load_lds_dwordx4 v[224:225], off
	v_lshl_add_u64 v[224:225], s[30:31], 0, v[132:133]
	s_mov_b32 m0, s33
	s_nop 0
	global_load_lds_dwordx4 v[224:225], off
	s_waitcnt vmcnt(8)
	s_waitcnt lgkmcnt(0)
	s_barrier
	s_waitcnt lgkmcnt(0)
	v_mfma_f32_16x16x32_bf16 v[126:129], v[152:155], v[184:187], v[126:129]
	v_mfma_f32_16x16x32_bf16 v[122:125], v[160:163], v[184:187], v[122:125]
	v_mfma_f32_16x16x32_bf16 v[118:121], v[152:155], v[192:195], v[118:121]
	v_mfma_f32_16x16x32_bf16 v[114:117], v[160:163], v[192:195], v[114:117]
	v_mfma_f32_16x16x32_bf16 v[102:105], v[152:155], v[200:203], v[102:105]
	v_mfma_f32_16x16x32_bf16 v[98:101], v[160:163], v[200:203], v[98:101]
	v_mfma_f32_16x16x32_bf16 v[86:89], v[152:155], v[208:211], v[86:89]
	v_mfma_f32_16x16x32_bf16 v[82:85], v[160:163], v[208:211], v[82:85]
	v_mfma_f32_16x16x32_bf16 v[126:129], v[156:159], v[188:191], v[126:129]
	v_mfma_f32_16x16x32_bf16 v[122:125], v[164:167], v[188:191], v[122:125]
	v_mfma_f32_16x16x32_bf16 v[118:121], v[156:159], v[196:199], v[118:121]
	v_mfma_f32_16x16x32_bf16 v[114:117], v[164:167], v[196:199], v[114:117]
	v_mfma_f32_16x16x32_bf16 v[102:105], v[156:159], v[204:207], v[102:105]
	v_mfma_f32_16x16x32_bf16 v[98:101], v[164:167], v[204:207], v[98:101]
	v_mfma_f32_16x16x32_bf16 v[86:89], v[156:159], v[212:215], v[86:89]
	v_mfma_f32_16x16x32_bf16 v[82:85], v[164:167], v[212:215], v[82:85]
	v_mfma_f32_16x16x32_bf16 v[110:113], v[168:171], v[184:187], v[110:113]
	v_mfma_f32_16x16x32_bf16 v[106:109], v[176:179], v[184:187], v[106:109]
	v_mfma_f32_16x16x32_bf16 v[94:97], v[168:171], v[192:195], v[94:97]
	v_mfma_f32_16x16x32_bf16 v[90:93], v[176:179], v[192:195], v[90:93]
	v_mfma_f32_16x16x32_bf16 v[78:81], v[168:171], v[200:203], v[78:81]
	v_mfma_f32_16x16x32_bf16 v[74:77], v[176:179], v[200:203], v[74:77]
	v_mfma_f32_16x16x32_bf16 v[70:73], v[168:171], v[208:211], v[70:73]
	v_mfma_f32_16x16x32_bf16 v[66:69], v[176:179], v[208:211], v[66:69]
	v_mfma_f32_16x16x32_bf16 v[110:113], v[172:175], v[188:191], v[110:113]
	v_mfma_f32_16x16x32_bf16 v[106:109], v[180:183], v[188:191], v[106:109]
	v_mfma_f32_16x16x32_bf16 v[94:97], v[172:175], v[196:199], v[94:97]
	v_mfma_f32_16x16x32_bf16 v[90:93], v[180:183], v[196:199], v[90:93]
	v_mfma_f32_16x16x32_bf16 v[78:81], v[172:175], v[204:207], v[78:81]
	v_mfma_f32_16x16x32_bf16 v[74:77], v[180:183], v[204:207], v[74:77]
	v_mfma_f32_16x16x32_bf16 v[70:73], v[172:175], v[212:215], v[70:73]
	v_mfma_f32_16x16x32_bf16 v[66:69], v[180:183], v[212:215], v[66:69]
	s_barrier
; #define PG8_STAGE_B(b, h, bp) PG8_STAGE2(PG8_SB(b, h), (bp) + (h) * hstepB, voffB[0], voffB[1])
; #define PG8_STAGE_A(b, h, ap, NX) do { if constexpr (GATHER) { const unsigned _o0 = (NX) ? vn[h][0] : vc[h][0], _o1 = (NX) ? vn[h][1] : vc[h][1]; PG8_STAGE2(PG8_SA(b, h), (ap), _o0, _o1); } \
;         else { PG8_STAGE2(PG8_SA(b, h), (ap) + (h) * hstepA, voffA[0], voffA[1]); } } while (0)
; #define PG8_LDA(dst, b, h) do { _Pragma("unroll") for (int m = 0; m < 4; ++m) _Pragma("unroll") for (int k = 0; k < 2; ++k) dst[m][k] = *(const LAS bf16x8*)(lds + PG8_SA(b, h) + aoff + m * 2048 + k * 1024); } while (0)
; #define PG8_MMA(ai, bj, At, Bt) do { __builtin_amdgcn_s_setprio(1); _Pragma("unroll") for (int m = 0; m < 4; ++m) _Pragma("unroll") for (int n = 0; n < 2; ++n) _Pragma("unroll") for (int k = 0; k < 2; ++k) \
;         acc[ai][bj][m][n] = __builtin_amdgcn_mfma_f32_16x16x32_bf16(Bt[n][k], At[m][k], acc[ai][bj][m][n], 0, 0, 0); __builtin_amdgcn_s_setprio(0); } while (0)
; #define PG8_WAIT_V(n) asm volatile("s_waitcnt vmcnt(" #n ")" ::: "memory")
; #define PG8_WAIT_L(n) asm volatile("s_waitcnt lgkmcnt(" #n ")" ::: "memory")
; #define PG8_BAR __builtin_amdgcn_s_barrier()
; #define PG8_SCHED __builtin_amdgcn_sched_barrier(0)
; template <class Epi, class Sched, bool GATHER, bool LIGHTSKIP = false>
; __device__ __forceinline__ void gemm_phase(LAS unsigned char* lds, LAS unsigned char* xl, const int lda, const int ldb, const int K, const Sched& S, const Epi& E) {
;     ...
;             PG8_LDA(At, 1, 1); PG8_STAGE_B(1, 0, b3); PG8_STAGE_B(1, 1, b3); PG8_STAGE_A(1, 0, a3, last);
;             PG8_WAIT_V(8); PG8_WAIT_L(0); PG8_BAR; if (!light) { PG8_MMA(1, 0, At, B0); PG8_MMA(1, 1, At, B1); } PG8_BAR; PG8_SCHED;
;         }
	s_add_i32 s30, s48, s4
	v_lshl_add_u64 v[216:217], v[216:217], 0, s[14:15]
	s_mov_b32 m0, s30
	ds_read_b128 v[184:187], v150 offset:49152
	ds_read_b128 v[188:191], v150 offset:50176
	ds_read_b128 v[192:195], v150 offset:51200
	ds_read_b128 v[196:199], v150 offset:52224
	ds_read_b128 v[200:203], v150 offset:53248
	ds_read_b128 v[204:207], v150 offset:54272
	ds_read_b128 v[208:211], v150 offset:55296
	ds_read_b128 v[212:215], v150 offset:56320
	global_load_lds_dwordx4 v[216:217], off
	s_add_i32 m0, s30, 0x2000
	s_add_u32 s28, s28, 0x80080
	v_lshl_add_u64 v[216:217], v[218:219], 0, s[14:15]
	s_addc_u32 s29, s29, 0
	s_add_i32 s30, s49, s4
	global_load_lds_dwordx4 v[216:217], off
	v_lshl_add_u64 v[216:217], s[28:29], 0, v[134:135]
	s_mov_b32 m0, s30
	s_nop 0
	global_load_lds_dwordx4 v[216:217], off
	v_lshl_add_u64 v[216:217], s[28:29], 0, v[130:131]
	s_add_i32 m0, s30, 0x2000
	s_nop 0
	global_load_lds_dwordx4 v[216:217], off
	v_lshl_add_u64 v[216:217], v[220:221], 0, s[14:15]
	s_mov_b32 m0, s35
	s_nop 0
	global_load_lds_dwordx4 v[216:217], off
	v_lshl_add_u64 v[216:217], v[222:223], 0, s[14:15]
	s_mov_b32 m0, s36
	s_nop 0
	global_load_lds_dwordx4 v[216:217], off
	s_waitcnt vmcnt(8)
	s_waitcnt lgkmcnt(0)
	s_barrier
	s_waitcnt lgkmcnt(0)
	v_mfma_f32_16x16x32_bf16 v[62:65], v[152:155], v[184:187], v[62:65]
	v_mfma_f32_16x16x32_bf16 v[58:61], v[160:163], v[184:187], v[58:61]
	v_mfma_f32_16x16x32_bf16 v[54:57], v[152:155], v[192:195], v[54:57]
	v_mfma_f32_16x16x32_bf16 v[50:53], v[160:163], v[192:195], v[50:53]
	v_mfma_f32_16x16x32_bf16 v[38:41], v[152:155], v[200:203], v[38:41]
	v_mfma_f32_16x16x32_bf16 v[34:37], v[160:163], v[200:203], v[34:37]
	v_mfma_f32_16x16x32_bf16 v[22:25], v[152:155], v[208:211], v[22:25]
	v_mfma_f32_16x16x32_bf16 v[18:21], v[160:163], v[208:211], v[18:21]
	v_mfma_f32_16x16x32_bf16 v[62:65], v[156:159], v[188:191], v[62:65]
	v_mfma_f32_16x16x32_bf16 v[58:61], v[164:167], v[188:191], v[58:61]
	v_mfma_f32_16x16x32_bf16 v[54:57], v[156:159], v[196:199], v[54:57]
	v_mfma_f32_16x16x32_bf16 v[50:53], v[164:167], v[196:199], v[50:53]
	v_mfma_f32_16x16x32_bf16 v[38:41], v[156:159], v[204:207], v[38:41]
	v_mfma_f32_16x16x32_bf16 v[34:37], v[164:167], v[204:207], v[34:37]
	v_mfma_f32_16x16x32_bf16 v[22:25], v[156:159], v[212:215], v[22:25]
	v_mfma_f32_16x16x32_bf16 v[18:21], v[164:167], v[212:215], v[18:21]
	v_mfma_f32_16x16x32_bf16 v[46:49], v[168:171], v[184:187], v[46:49]
	v_mfma_f32_16x16x32_bf16 v[42:45], v[176:179], v[184:187], v[42:45]
	v_mfma_f32_16x16x32_bf16 v[30:33], v[168:171], v[192:195], v[30:33]
	v_mfma_f32_16x16x32_bf16 v[26:29], v[176:179], v[192:195], v[26:29]
	v_mfma_f32_16x16x32_bf16 v[14:17], v[168:171], v[200:203], v[14:17]
	v_mfma_f32_16x16x32_bf16 v[10:13], v[176:179], v[200:203], v[10:13]
	v_mfma_f32_16x16x32_bf16 v[6:9], v[168:171], v[208:211], v[6:9]
	v_mfma_f32_16x16x32_bf16 v[2:5], v[176:179], v[208:211], v[2:5]
	v_mfma_f32_16x16x32_bf16 v[46:49], v[172:175], v[188:191], v[46:49]
	v_mfma_f32_16x16x32_bf16 v[42:45], v[180:183], v[188:191], v[42:45]
	v_mfma_f32_16x16x32_bf16 v[30:33], v[172:175], v[196:199], v[30:33]
	v_mfma_f32_16x16x32_bf16 v[26:29], v[180:183], v[196:199], v[26:29]
	v_mfma_f32_16x16x32_bf16 v[14:17], v[172:175], v[204:207], v[14:17]
	v_mfma_f32_16x16x32_bf16 v[10:13], v[180:183], v[204:207], v[10:13]
	v_mfma_f32_16x16x32_bf16 v[6:9], v[172:175], v[212:215], v[6:9]
	v_mfma_f32_16x16x32_bf16 v[2:5], v[180:183], v[212:215], v[2:5]
	s_barrier
	s_add_i32 s47, s47, 2
	s_add_u32 s22, s22, 0x100
	s_addc_u32 s23, s23, 0
	s_add_u32 s45, s45, 0x100
	s_addc_u32 s46, s46, 0
	s_cmp_gt_u32 s47, 29
	s_cbranch_scc0 .LBB0_153
	s_branch .Lpeel_exit_0

; __device__ __forceinline__ unsigned cvt_pk_bf16(float lo, float hi) { const f32x2 v = {lo, hi}; return __builtin_bit_cast(unsigned, __builtin_convertvector(v, bf16x2_t)); }
; #define PG8_BAR __builtin_amdgcn_s_barrier()
; template <class Epi, class Sched, bool GATHER, bool LIGHTSKIP = false>
; __device__ __forceinline__ void gemm_phase(LAS unsigned char* lds, LAS unsigned char* xl, const int lda, const int ldb, const int K, const Sched& S, const Epi& E) {
;     ...
;         if (wr == 0) PG8_BAR;
;         E(acc, cur, wr, wc, fr, fq, xl, wid, lane);
;         if (!has_next) break;
; #pragma unroll
;         for (int a = 0; a < 2; ++a)
; #pragma unroll
;             for (int b = 0; b < 2; ++b)
; #pragma unroll
;                 for (int m = 0; m < 4; ++m)
; #pragma unroll
;                     for (int n = 0; n < 2; ++n) acc[a][b][m][n] = (f32x4){0.f, 0.f, 0.f, 0.f};
;         cur = nxt; cA = nA; cB = nB; ++ui;
;         if constexpr (GATHER) {
; #pragma unroll
;             for (int h = 0; h < 2; ++h) { vc[h][0] = vn[h][0]; vc[h][1] = vn[h][1]; } }
;         if (wr == 1) PG8_BAR;
;     __device__ __forceinline__ void operator()(Acc& acc, const GUnit& u, int wr, int wc, int fr, int fq, LAS unsigned char*, int, int) const {
;         const int row0 = u.x0 + wr * 64 + fr, col0 = u.x1 + wc * 32 + 8 * fq;
; #pragma unroll
;         for (int ai = 0; ai < 2; ++ai)
; #pragma unroll
;             for (int m = 0; m < 4; ++m) { bf16_t* rowp = O + (size_t)(row0 + ai * HALF + m * 16) * ldc + col0;
; #pragma unroll
;                 for (int bj = 0; bj < 2; ++bj) { const f32x4 v0 = acc[ai][bj][m][0], v1 = acc[ai][bj][m][1];
;                     u32x4 w; w.x = cvt_pk_bf16(v0[0], v0[1]); w.y = cvt_pk_bf16(v0[2], v0[3]); w.z = cvt_pk_bf16(v1[0], v1[1]); w.w = cvt_pk_bf16(v1[2], v1[3]);
;                     if constexpr (NT) __builtin_nontemporal_store(w, (u32x4*)(rowp + bj * HALF)); else *(u32x4*)(rowp + bj * HALF) = w; } }
.Lpeel_exit_0:
	s_and_b64 vcc, exec, s[16:17]
	s_cbranch_vccz .LBB0_156
	s_and_b64 vcc, exec, s[8:9]
	s_cbranch_vccnz .LBB0_156
	s_barrier
.LBB0_156:
	v_add_u32_e32 v151, s44, v1
	v_add_u32_e32 v152, s43, v147
	v_ashrrev_i32_e32 v153, 31, v152
	v_mov_b64_e32 v[154:155], s[12:13]
	v_cvt_pk_bf16_f32 v70, v70, v71
	v_cvt_pk_bf16_f32 v71, v72, v73
	v_cvt_pk_bf16_f32 v72, v66, v67
	v_add_u32_e32 v66, 0x80, v151
	v_mad_i64_i32 v[156:157], s[22:23], v151, s40, v[154:155]
	v_lshlrev_b64 v[152:153], 1, v[152:153]
	v_cvt_pk_bf16_f32 v110, v110, v111
	v_cvt_pk_bf16_f32 v111, v112, v113
	v_cvt_pk_bf16_f32 v112, v106, v107
	v_add_u32_e32 v106, 16, v151
	v_mad_i64_i32 v[66:67], s[22:23], v66, s40, v[154:155]
	v_cvt_pk_bf16_f32 v46, v46, v47
	v_cvt_pk_bf16_f32 v47, v48, v49
	v_cvt_pk_bf16_f32 v48, v42, v43
	v_add_u32_e32 v42, 0x90, v151
	v_lshl_add_u64 v[156:157], v[156:157], 0, v[152:153]
	v_cvt_pk_bf16_f32 v113, v108, v109
	v_mad_i64_i32 v[106:107], s[22:23], v106, s40, v[154:155]
	v_cvt_pk_bf16_f32 v94, v94, v95
	v_cvt_pk_bf16_f32 v95, v96, v97
	v_cvt_pk_bf16_f32 v96, v90, v91
	v_add_u32_e32 v90, 32, v151
	v_lshl_add_u64 v[66:67], v[66:67], 0, v[152:153]
	v_cvt_pk_bf16_f32 v49, v44, v45
	v_mad_i64_i32 v[42:43], s[22:23], v42, s40, v[154:155]
	v_cvt_pk_bf16_f32 v30, v30, v31
	v_cvt_pk_bf16_f32 v31, v32, v33
	v_cvt_pk_bf16_f32 v32, v26, v27
	v_add_u32_e32 v26, 0xa0, v151
	global_store_dwordx4 v[156:157], v[110:113], off offset:256
	v_cvt_pk_bf16_f32 v97, v92, v93
	v_mad_i64_i32 v[90:91], s[22:23], v90, s40, v[154:155]
	v_lshl_add_u64 v[110:111], v[106:107], 0, v[152:153]
	v_cvt_pk_bf16_f32 v78, v78, v79
	v_cvt_pk_bf16_f32 v79, v80, v81
	v_cvt_pk_bf16_f32 v80, v74, v75
	v_add_u32_e32 v74, 48, v151
	global_store_dwordx4 v[66:67], v[46:49], off offset:256
	v_cvt_pk_bf16_f32 v33, v28, v29
	v_mad_i64_i32 v[26:27], s[22:23], v26, s40, v[154:155]
	v_lshl_add_u64 v[46:47], v[42:43], 0, v[152:153]
	v_cvt_pk_bf16_f32 v14, v14, v15
	v_cvt_pk_bf16_f32 v15, v16, v17
	v_cvt_pk_bf16_f32 v16, v10, v11
	v_add_u32_e32 v10, 0xb0, v151
	global_store_dwordx4 v[110:111], v[94:97], off offset:256
	v_cvt_pk_bf16_f32 v81, v76, v77
	v_mad_i64_i32 v[74:75], s[22:23], v74, s40, v[154:155]
	v_lshl_add_u64 v[94:95], v[90:91], 0, v[152:153]
	global_store_dwordx4 v[46:47], v[30:33], off offset:256
	v_cvt_pk_bf16_f32 v17, v12, v13
	v_mad_i64_i32 v[10:11], s[22:23], v10, s40, v[154:155]
	v_lshl_add_u64 v[30:31], v[26:27], 0, v[152:153]
	v_cvt_pk_bf16_f32 v126, v126, v127
	v_cvt_pk_bf16_f32 v127, v128, v129
	v_cvt_pk_bf16_f32 v128, v122, v123
	v_cvt_pk_bf16_f32 v129, v124, v125
	v_cvt_pk_bf16_f32 v106, v118, v119
	v_cvt_pk_bf16_f32 v107, v120, v121
	v_cvt_pk_bf16_f32 v108, v114, v115
	v_cvt_pk_bf16_f32 v109, v116, v117
	v_cvt_pk_bf16_f32 v90, v102, v103
	v_cvt_pk_bf16_f32 v91, v104, v105
	v_cvt_pk_bf16_f32 v92, v98, v99
	v_cvt_pk_bf16_f32 v93, v100, v101
	global_store_dwordx4 v[94:95], v[78:81], off offset:256
	v_cvt_pk_bf16_f32 v76, v82, v83
	v_cvt_pk_bf16_f32 v77, v84, v85
	v_lshl_add_u64 v[78:79], v[74:75], 0, v[152:153]
	v_cvt_pk_bf16_f32 v74, v86, v87
	v_cvt_pk_bf16_f32 v75, v88, v89
	v_cvt_pk_bf16_f32 v73, v68, v69
	v_cvt_pk_bf16_f32 v62, v62, v63
	v_cvt_pk_bf16_f32 v63, v64, v65
	v_cvt_pk_bf16_f32 v64, v58, v59
	v_cvt_pk_bf16_f32 v65, v60, v61
	v_cvt_pk_bf16_f32 v42, v54, v55
	v_cvt_pk_bf16_f32 v43, v56, v57
	v_cvt_pk_bf16_f32 v44, v50, v51
	v_cvt_pk_bf16_f32 v45, v52, v53
	v_cvt_pk_bf16_f32 v26, v38, v39
	v_cvt_pk_bf16_f32 v27, v40, v41
	v_cvt_pk_bf16_f32 v28, v34, v35
	v_cvt_pk_bf16_f32 v29, v36, v37
	global_store_dwordx4 v[30:31], v[14:17], off offset:256
	v_cvt_pk_bf16_f32 v12, v18, v19
	v_cvt_pk_bf16_f32 v13, v20, v21
	v_lshl_add_u64 v[14:15], v[10:11], 0, v[152:153]
	v_cvt_pk_bf16_f32 v10, v22, v23
	v_cvt_pk_bf16_f32 v11, v24, v25
	v_cvt_pk_bf16_f32 v6, v6, v7
	v_cvt_pk_bf16_f32 v7, v8, v9
	v_cvt_pk_bf16_f32 v8, v2, v3
	v_cvt_pk_bf16_f32 v9, v4, v5
	s_andn2_b64 vcc, exec, s[8:9]
	s_mov_b64 s[8:9], -1
	global_store_dwordx4 v[156:157], v[126:129], off
	global_store_dwordx4 v[110:111], v[106:109], off
	global_store_dwordx4 v[94:95], v[90:93], off
	global_store_dwordx4 v[78:79], v[74:77], off
	global_store_dwordx4 v[78:79], v[70:73], off offset:256
	global_store_dwordx4 v[66:67], v[62:65], off
	global_store_dwordx4 v[46:47], v[42:45], off
	global_store_dwordx4 v[30:31], v[26:29], off
	global_store_dwordx4 v[14:15], v[10:13], off
	global_store_dwordx4 v[14:15], v[6:9], off offset:256
	s_cbranch_vccnz .LBB0_149
	s_andn2_b64 vcc, exec, s[10:11]
	s_cbranch_vccnz .LBB0_148
	s_nop 0
	s_branch .LBB0_148

; #define PG8_STAGE_B(b, h, bp) PG8_STAGE2(PG8_SB(b, h), (bp) + (h) * hstepB, voffB[0], voffB[1])
; #define PG8_STAGE_A(b, h, ap, NX) do { if constexpr (GATHER) { const unsigned _o0 = (NX) ? vn[h][0] : vc[h][0], _o1 = (NX) ? vn[h][1] : vc[h][1]; PG8_STAGE2(PG8_SA(b, h), (ap), _o0, _o1); } \
;         else { PG8_STAGE2(PG8_SA(b, h), (ap) + (h) * hstepA, voffA[0], voffA[1]); } } while (0)
; #define PG8_LDA(dst, b, h) do { _Pragma("unroll") for (int m = 0; m < 4; ++m) _Pragma("unroll") for (int k = 0; k < 2; ++k) dst[m][k] = *(const LAS bf16x8*)(lds + PG8_SA(b, h) + aoff + m * 2048 + k * 1024); } while (0)
; #define PG8_LDB(dst, b, h) do { _Pragma("unroll") for (int n = 0; n < 2; ++n) _Pragma("unroll") for (int k = 0; k < 2; ++k) dst[n][k] = *(const LAS bf16x8*)(lds + PG8_SB(b, h) + boff + n * 2048 + k * 1024); } while (0)
; #define PG8_MMA(ai, bj, At, Bt) do { __builtin_amdgcn_s_setprio(1); _Pragma("unroll") for (int m = 0; m < 4; ++m) _Pragma("unroll") for (int n = 0; n < 2; ++n) _Pragma("unroll") for (int k = 0; k < 2; ++k) \
;         acc[ai][bj][m][n] = __builtin_amdgcn_mfma_f32_16x16x32_bf16(Bt[n][k], At[m][k], acc[ai][bj][m][n], 0, 0, 0); __builtin_amdgcn_s_setprio(0); } while (0)
; #define PG8_WAIT_V(n) asm volatile("s_waitcnt vmcnt(" #n ")" ::: "memory")
; template <class Epi, class Sched, bool GATHER, bool LIGHTSKIP = false>
; __device__ __forceinline__ void gemm_phase(LAS unsigned char* lds, LAS unsigned char* xl, const int lda, const int ldb, const int K, const Sched& S, const Epi& E) {
;     ...
;     GUnit cur, nxt; int ui = 0;
;     if (!S.next(0, cur)) return;
;     Acc acc;
; #pragma unroll
;     for (int a = 0; a < 2; ++a)
; #pragma unroll
;         for (int b = 0; b < 2; ++b)
; #pragma unroll
;             for (int m = 0; m < 4; ++m)
; #pragma unroll
;                 for (int n = 0; n < 2; ++n) acc[a][b][m][n] = (f32x4){0.f, 0.f, 0.f, 0.f};
;     ...
;             PG8_LDB(B0, 0, 0); PG8_LDB(B1, 0, 1); PG8_SCHED; PG8_LDA(At, 0, 0); PG8_STAGE_A(1, 1, a1, false);
;             PG8_WAIT_V(8); PG8_WAIT_L(0); PG8_BAR; PG8_MMA(0, 0, At, B0); PG8_MMA(0, 1, At, B1); PG8_BAR; PG8_SCHED;
;             PG8_LDA(At, 0, 1); PG8_STAGE_B(0, 0, b2); PG8_STAGE_B(0, 1, b2); PG8_STAGE_A(0, 0, a2, last);
;             PG8_WAIT_V(8); PG8_WAIT_L(0); PG8_BAR; if (!light) { PG8_MMA(1, 0, At, B0); PG8_MMA(1, 1, At, B1); } PG8_BAR; PG8_SCHED;
.LBB0_829:
	s_add_u32 s40, s40, 0x80080
	s_addc_u32 s41, s41, 0
	s_add_u32 s55, s42, 0x100
	s_addc_u32 s56, s43, 0
	s_mov_b32 s57, -2
	ds_read_b128 v[146:149], v152
	ds_read_b128 v[156:159], v152 offset:1024
	ds_read_b128 v[160:163], v152 offset:2048
	ds_read_b128 v[164:167], v152 offset:3072
	ds_read_b128 v[168:171], v153
	ds_read_b128 v[172:175], v153 offset:1024
	ds_read_b128 v[176:179], v153 offset:2048
	ds_read_b128 v[180:183], v153 offset:3072
	s_add_u32 s42, s40, 0xfff80080
	s_addc_u32 s43, s41, -1
	s_cmp_eq_u32 s57, 28
	s_cselect_b32 s45, s37, s43
	s_cselect_b32 s44, s36, s42
	s_cselect_b32 s43, s39, s56
	s_cselect_b32 s42, s38, s55
	v_lshl_add_u64 v[216:217], s[40:41], 0, v[138:139]
	s_add_i32 m0, s6, 0xc000
	ds_read_b128 v[184:187], v154
	ds_read_b128 v[188:191], v154 offset:1024
	ds_read_b128 v[192:195], v154 offset:2048
	ds_read_b128 v[196:199], v154 offset:3072
	ds_read_b128 v[200:203], v154 offset:4096
	ds_read_b128 v[204:207], v154 offset:5120
	ds_read_b128 v[208:211], v154 offset:6144
	ds_read_b128 v[212:215], v154 offset:7168
	global_load_lds_dwordx4 v[216:217], off
	v_lshl_add_u64 v[216:217], s[40:41], 0, v[140:141]
	s_add_i32 m0, s6, 0xe000
	s_nop 0
	global_load_lds_dwordx4 v[216:217], off
	s_waitcnt vmcnt(8)
	s_waitcnt lgkmcnt(0)
	s_barrier
	s_waitcnt lgkmcnt(0)
	v_mfma_f32_16x16x32_bf16 v[126:129], v[146:149], v[184:187], 0
	v_mfma_f32_16x16x32_bf16 v[122:125], v[160:163], v[184:187], 0
	v_mfma_f32_16x16x32_bf16 v[110:113], v[146:149], v[192:195], 0
	v_mfma_f32_16x16x32_bf16 v[106:109], v[160:163], v[192:195], 0
	v_mfma_f32_16x16x32_bf16 v[94:97], v[146:149], v[200:203], 0
	v_mfma_f32_16x16x32_bf16 v[90:93], v[160:163], v[200:203], 0
	v_mfma_f32_16x16x32_bf16 v[78:81], v[146:149], v[208:211], 0
	v_mfma_f32_16x16x32_bf16 v[74:77], v[160:163], v[208:211], 0
	v_mfma_f32_16x16x32_bf16 v[126:129], v[156:159], v[188:191], v[126:129]
	v_mfma_f32_16x16x32_bf16 v[122:125], v[164:167], v[188:191], v[122:125]
	v_mfma_f32_16x16x32_bf16 v[110:113], v[156:159], v[196:199], v[110:113]
	v_mfma_f32_16x16x32_bf16 v[106:109], v[164:167], v[196:199], v[106:109]
	v_mfma_f32_16x16x32_bf16 v[94:97], v[156:159], v[204:207], v[94:97]
	v_mfma_f32_16x16x32_bf16 v[90:93], v[164:167], v[204:207], v[90:93]
	v_mfma_f32_16x16x32_bf16 v[78:81], v[156:159], v[212:215], v[78:81]
	v_mfma_f32_16x16x32_bf16 v[74:77], v[164:167], v[212:215], v[74:77]
	v_mfma_f32_16x16x32_bf16 v[118:121], v[168:171], v[184:187], 0
	v_mfma_f32_16x16x32_bf16 v[114:117], v[176:179], v[184:187], 0
	v_mfma_f32_16x16x32_bf16 v[102:105], v[168:171], v[192:195], 0
	v_mfma_f32_16x16x32_bf16 v[98:101], v[176:179], v[192:195], 0
	v_mfma_f32_16x16x32_bf16 v[86:89], v[168:171], v[200:203], 0
	v_mfma_f32_16x16x32_bf16 v[82:85], v[176:179], v[200:203], 0
	v_mfma_f32_16x16x32_bf16 v[70:73], v[168:171], v[208:211], 0
	v_mfma_f32_16x16x32_bf16 v[66:69], v[176:179], v[208:211], 0
	v_mfma_f32_16x16x32_bf16 v[118:121], v[172:175], v[188:191], v[118:121]
	v_mfma_f32_16x16x32_bf16 v[114:117], v[180:183], v[188:191], v[114:117]
	v_mfma_f32_16x16x32_bf16 v[102:105], v[172:175], v[196:199], v[102:105]
	v_mfma_f32_16x16x32_bf16 v[98:101], v[180:183], v[196:199], v[98:101]
	v_mfma_f32_16x16x32_bf16 v[86:89], v[172:175], v[204:207], v[86:89]
	v_mfma_f32_16x16x32_bf16 v[82:85], v[180:183], v[204:207], v[82:85]
	v_mfma_f32_16x16x32_bf16 v[70:73], v[172:175], v[212:215], v[70:73]
	v_mfma_f32_16x16x32_bf16 v[66:69], v[180:183], v[212:215], v[66:69]
	s_barrier
	s_add_i32 s58, s50, s5
	v_lshl_add_u64 v[216:217], s[42:43], 0, v[132:133]
	s_mov_b32 m0, s58
	ds_read_b128 v[184:187], v154 offset:16384
	ds_read_b128 v[188:191], v154 offset:17408
	ds_read_b128 v[192:195], v154 offset:18432
	ds_read_b128 v[196:199], v154 offset:19456
	ds_read_b128 v[200:203], v154 offset:20480
	ds_read_b128 v[204:207], v154 offset:21504
	ds_read_b128 v[208:211], v154 offset:22528
	ds_read_b128 v[212:215], v154 offset:23552
	global_load_lds_dwordx4 v[216:217], off
	s_add_i32 m0, s58, 0x2000
	s_add_u32 s58, s42, 0x80000
	v_lshl_add_u64 v[218:219], s[42:43], 0, v[136:137]
	s_addc_u32 s59, s43, 0
	s_add_i32 s60, s51, s5
	global_load_lds_dwordx4 v[218:219], off
	v_lshl_add_u64 v[220:221], s[58:59], 0, v[132:133]
	s_mov_b32 m0, s60
	v_lshl_add_u64 v[222:223], s[44:45], 0, v[134:135]
	global_load_lds_dwordx4 v[220:221], off
	v_lshl_add_u64 v[220:221], s[58:59], 0, v[136:137]
	s_add_i32 m0, s60, 0x2000
	s_nop 0
	global_load_lds_dwordx4 v[220:221], off
	v_lshl_add_u64 v[220:221], s[44:45], 0, v[130:131]
	s_mov_b32 m0, s6
	s_nop 0
	global_load_lds_dwordx4 v[220:221], off
	s_mov_b32 m0, s7
	s_nop 0
	global_load_lds_dwordx4 v[222:223], off
	s_waitcnt vmcnt(8)
	s_waitcnt lgkmcnt(0)
	s_barrier
; #define PG8_STAGE_A(b, h, ap, NX) do { if constexpr (GATHER) { const unsigned _o0 = (NX) ? vn[h][0] : vc[h][0], _o1 = (NX) ? vn[h][1] : vc[h][1]; PG8_STAGE2(PG8_SA(b, h), (ap), _o0, _o1); } \
;         else { PG8_STAGE2(PG8_SA(b, h), (ap) + (h) * hstepA, voffA[0], voffA[1]); } } while (0)
; #define PG8_LDA(dst, b, h) do { _Pragma("unroll") for (int m = 0; m < 4; ++m) _Pragma("unroll") for (int k = 0; k < 2; ++k) dst[m][k] = *(const LAS bf16x8*)(lds + PG8_SA(b, h) + aoff + m * 2048 + k * 1024); } while (0)
; #define PG8_LDB(dst, b, h) do { _Pragma("unroll") for (int n = 0; n < 2; ++n) _Pragma("unroll") for (int k = 0; k < 2; ++k) dst[n][k] = *(const LAS bf16x8*)(lds + PG8_SB(b, h) + boff + n * 2048 + k * 1024); } while (0)
; #define PG8_MMA(ai, bj, At, Bt) do { __builtin_amdgcn_s_setprio(1); _Pragma("unroll") for (int m = 0; m < 4; ++m) _Pragma("unroll") for (int n = 0; n < 2; ++n) _Pragma("unroll") for (int k = 0; k < 2; ++k) \
;         acc[ai][bj][m][n] = __builtin_amdgcn_mfma_f32_16x16x32_bf16(Bt[n][k], At[m][k], acc[ai][bj][m][n], 0, 0, 0); __builtin_amdgcn_s_setprio(0); } while (0)
; #define PG8_WAIT_V(n) asm volatile("s_waitcnt vmcnt(" #n ")" ::: "memory")
; #define PG8_WAIT_L(n) asm volatile("s_waitcnt lgkmcnt(" #n ")" ::: "memory")
; #define PG8_BAR __builtin_amdgcn_s_barrier()
; #define PG8_SCHED __builtin_amdgcn_sched_barrier(0)
; template <class Epi, class Sched, bool GATHER, bool LIGHTSKIP = false>
; __device__ __forceinline__ void gemm_phase(LAS unsigned char* lds, LAS unsigned char* xl, const int lda, const int ldb, const int K, const Sched& S, const Epi& E) {
;     ...
;             PG8_WAIT_V(8); PG8_WAIT_L(0); PG8_BAR; if (!light) { PG8_MMA(1, 0, At, B0); PG8_MMA(1, 1, At, B1); } PG8_BAR; PG8_SCHED;
;             PG8_LDB(B0, 1, 0); PG8_LDB(B1, 1, 1); PG8_SCHED; PG8_LDA(At, 1, 0); PG8_STAGE_A(0, 1, a2, last);
;             PG8_WAIT_V(8); PG8_WAIT_L(0); PG8_BAR; PG8_MMA(0, 0, At, B0); PG8_MMA(0, 1, At, B1); PG8_BAR; PG8_SCHED;
	s_waitcnt lgkmcnt(0)
	v_mfma_f32_16x16x32_bf16 v[62:65], v[146:149], v[184:187], 0
	v_mfma_f32_16x16x32_bf16 v[58:61], v[160:163], v[184:187], 0
	v_mfma_f32_16x16x32_bf16 v[46:49], v[146:149], v[192:195], 0
	v_mfma_f32_16x16x32_bf16 v[42:45], v[160:163], v[192:195], 0
	v_mfma_f32_16x16x32_bf16 v[30:33], v[146:149], v[200:203], 0
	v_mfma_f32_16x16x32_bf16 v[26:29], v[160:163], v[200:203], 0
	v_mfma_f32_16x16x32_bf16 v[14:17], v[146:149], v[208:211], 0
	v_mfma_f32_16x16x32_bf16 v[10:13], v[160:163], v[208:211], 0
	v_mfma_f32_16x16x32_bf16 v[62:65], v[156:159], v[188:191], v[62:65]
	v_mfma_f32_16x16x32_bf16 v[58:61], v[164:167], v[188:191], v[58:61]
	v_mfma_f32_16x16x32_bf16 v[46:49], v[156:159], v[196:199], v[46:49]
	v_mfma_f32_16x16x32_bf16 v[42:45], v[164:167], v[196:199], v[42:45]
	v_mfma_f32_16x16x32_bf16 v[30:33], v[156:159], v[204:207], v[30:33]
	v_mfma_f32_16x16x32_bf16 v[26:29], v[164:167], v[204:207], v[26:29]
	v_mfma_f32_16x16x32_bf16 v[14:17], v[156:159], v[212:215], v[14:17]
	v_mfma_f32_16x16x32_bf16 v[10:13], v[164:167], v[212:215], v[10:13]
	v_mfma_f32_16x16x32_bf16 v[54:57], v[168:171], v[184:187], 0
	v_mfma_f32_16x16x32_bf16 v[50:53], v[176:179], v[184:187], 0
	v_mfma_f32_16x16x32_bf16 v[38:41], v[168:171], v[192:195], 0
	v_mfma_f32_16x16x32_bf16 v[34:37], v[176:179], v[192:195], 0
	v_mfma_f32_16x16x32_bf16 v[22:25], v[168:171], v[200:203], 0
	v_mfma_f32_16x16x32_bf16 v[18:21], v[176:179], v[200:203], 0
	v_mfma_f32_16x16x32_bf16 v[6:9], v[168:171], v[208:211], 0
	v_mfma_f32_16x16x32_bf16 v[2:5], v[176:179], v[208:211], 0
	v_mfma_f32_16x16x32_bf16 v[54:57], v[172:175], v[188:191], v[54:57]
	v_mfma_f32_16x16x32_bf16 v[50:53], v[180:183], v[188:191], v[50:53]
	v_mfma_f32_16x16x32_bf16 v[38:41], v[172:175], v[196:199], v[38:41]
	v_mfma_f32_16x16x32_bf16 v[34:37], v[180:183], v[196:199], v[34:37]
	v_mfma_f32_16x16x32_bf16 v[22:25], v[172:175], v[204:207], v[22:25]
	v_mfma_f32_16x16x32_bf16 v[18:21], v[180:183], v[204:207], v[18:21]
	v_mfma_f32_16x16x32_bf16 v[6:9], v[172:175], v[212:215], v[6:9]
	v_mfma_f32_16x16x32_bf16 v[2:5], v[180:183], v[212:215], v[2:5]
	s_barrier
	s_add_i32 s58, 0, 0x18000
	v_add_u32_e32 v155, s58, v150
	s_add_i32 s59, 0, 0x1c000
	ds_read_b128 v[146:149], v155
	ds_read_b128 v[156:159], v155 offset:1024
	ds_read_b128 v[160:163], v155 offset:2048
	ds_read_b128 v[164:167], v155 offset:3072
	v_add_u32_e32 v155, s59, v150
	ds_read_b128 v[168:171], v155
	ds_read_b128 v[172:175], v155 offset:1024
	ds_read_b128 v[176:179], v155 offset:2048
	ds_read_b128 v[180:183], v155 offset:3072
	s_add_u32 s44, s44, 0x80000
	s_addc_u32 s45, s45, 0
	s_mov_b32 m0, s26
	v_lshl_add_u64 v[224:225], s[44:45], 0, v[130:131]
	ds_read_b128 v[184:187], v154 offset:32768
	ds_read_b128 v[188:191], v154 offset:33792
	ds_read_b128 v[192:195], v154 offset:34816
	ds_read_b128 v[196:199], v154 offset:35840
	ds_read_b128 v[200:203], v154 offset:36864
	ds_read_b128 v[204:207], v154 offset:37888
	ds_read_b128 v[208:211], v154 offset:38912
	ds_read_b128 v[212:215], v154 offset:39936
	global_load_lds_dwordx4 v[224:225], off
	v_lshl_add_u64 v[224:225], s[44:45], 0, v[134:135]
	s_mov_b32 m0, s27
	s_nop 0
	global_load_lds_dwordx4 v[224:225], off
	s_waitcnt vmcnt(8)
	s_waitcnt lgkmcnt(0)
	s_barrier
	s_waitcnt lgkmcnt(0)
	v_mfma_f32_16x16x32_bf16 v[126:129], v[146:149], v[184:187], v[126:129]
	v_mfma_f32_16x16x32_bf16 v[122:125], v[160:163], v[184:187], v[122:125]
	v_mfma_f32_16x16x32_bf16 v[110:113], v[146:149], v[192:195], v[110:113]
	v_mfma_f32_16x16x32_bf16 v[106:109], v[160:163], v[192:195], v[106:109]
	v_mfma_f32_16x16x32_bf16 v[94:97], v[146:149], v[200:203], v[94:97]
	v_mfma_f32_16x16x32_bf16 v[90:93], v[160:163], v[200:203], v[90:93]
	v_mfma_f32_16x16x32_bf16 v[78:81], v[146:149], v[208:211], v[78:81]
	v_mfma_f32_16x16x32_bf16 v[74:77], v[160:163], v[208:211], v[74:77]
	v_mfma_f32_16x16x32_bf16 v[126:129], v[156:159], v[188:191], v[126:129]
	v_mfma_f32_16x16x32_bf16 v[122:125], v[164:167], v[188:191], v[122:125]
	v_mfma_f32_16x16x32_bf16 v[110:113], v[156:159], v[196:199], v[110:113]
	v_mfma_f32_16x16x32_bf16 v[106:109], v[164:167], v[196:199], v[106:109]
	v_mfma_f32_16x16x32_bf16 v[94:97], v[156:159], v[204:207], v[94:97]
	v_mfma_f32_16x16x32_bf16 v[90:93], v[164:167], v[204:207], v[90:93]
	v_mfma_f32_16x16x32_bf16 v[78:81], v[156:159], v[212:215], v[78:81]
	v_mfma_f32_16x16x32_bf16 v[74:77], v[164:167], v[212:215], v[74:77]
	v_mfma_f32_16x16x32_bf16 v[118:121], v[168:171], v[184:187], v[118:121]
	v_mfma_f32_16x16x32_bf16 v[114:117], v[176:179], v[184:187], v[114:117]
	v_mfma_f32_16x16x32_bf16 v[102:105], v[168:171], v[192:195], v[102:105]
	v_mfma_f32_16x16x32_bf16 v[98:101], v[176:179], v[192:195], v[98:101]
	v_mfma_f32_16x16x32_bf16 v[86:89], v[168:171], v[200:203], v[86:89]
	v_mfma_f32_16x16x32_bf16 v[82:85], v[176:179], v[200:203], v[82:85]
	v_mfma_f32_16x16x32_bf16 v[70:73], v[168:171], v[208:211], v[70:73]
	v_mfma_f32_16x16x32_bf16 v[66:69], v[176:179], v[208:211], v[66:69]
	v_mfma_f32_16x16x32_bf16 v[118:121], v[172:175], v[188:191], v[118:121]
	v_mfma_f32_16x16x32_bf16 v[114:117], v[180:183], v[188:191], v[114:117]
	v_mfma_f32_16x16x32_bf16 v[102:105], v[172:175], v[196:199], v[102:105]
	v_mfma_f32_16x16x32_bf16 v[98:101], v[180:183], v[196:199], v[98:101]
	v_mfma_f32_16x16x32_bf16 v[86:89], v[172:175], v[204:207], v[86:89]
	v_mfma_f32_16x16x32_bf16 v[82:85], v[180:183], v[204:207], v[82:85]
	v_mfma_f32_16x16x32_bf16 v[70:73], v[172:175], v[212:215], v[70:73]
	v_mfma_f32_16x16x32_bf16 v[66:69], v[180:183], v[212:215], v[66:69]
	s_barrier
; #define PG8_STAGE_B(b, h, bp) PG8_STAGE2(PG8_SB(b, h), (bp) + (h) * hstepB, voffB[0], voffB[1])
; #define PG8_STAGE_A(b, h, ap, NX) do { if constexpr (GATHER) { const unsigned _o0 = (NX) ? vn[h][0] : vc[h][0], _o1 = (NX) ? vn[h][1] : vc[h][1]; PG8_STAGE2(PG8_SA(b, h), (ap), _o0, _o1); } \
;         else { PG8_STAGE2(PG8_SA(b, h), (ap) + (h) * hstepA, voffA[0], voffA[1]); } } while (0)
; #define PG8_LDA(dst, b, h) do { _Pragma("unroll") for (int m = 0; m < 4; ++m) _Pragma("unroll") for (int k = 0; k < 2; ++k) dst[m][k] = *(const LAS bf16x8*)(lds + PG8_SA(b, h) + aoff + m * 2048 + k * 1024); } while (0)
; #define PG8_MMA(ai, bj, At, Bt) do { __builtin_amdgcn_s_setprio(1); _Pragma("unroll") for (int m = 0; m < 4; ++m) _Pragma("unroll") for (int n = 0; n < 2; ++n) _Pragma("unroll") for (int k = 0; k < 2; ++k) \
;         acc[ai][bj][m][n] = __builtin_amdgcn_mfma_f32_16x16x32_bf16(Bt[n][k], At[m][k], acc[ai][bj][m][n], 0, 0, 0); __builtin_amdgcn_s_setprio(0); } while (0)
; #define PG8_WAIT_V(n) asm volatile("s_waitcnt vmcnt(" #n ")" ::: "memory")
; #define PG8_WAIT_L(n) asm volatile("s_waitcnt lgkmcnt(" #n ")" ::: "memory")
; #define PG8_BAR __builtin_amdgcn_s_barrier()
; #define PG8_SCHED __builtin_amdgcn_sched_barrier(0)
; template <class Epi, class Sched, bool GATHER, bool LIGHTSKIP = false>
; __device__ __forceinline__ void gemm_phase(LAS unsigned char* lds, LAS unsigned char* xl, const int lda, const int ldb, const int K, const Sched& S, const Epi& E) {
;     ...
;             PG8_LDA(At, 1, 1); PG8_STAGE_B(1, 0, b3); PG8_STAGE_B(1, 1, b3); PG8_STAGE_A(1, 0, a3, last);
;             PG8_WAIT_V(8); PG8_WAIT_L(0); PG8_BAR; if (!light) { PG8_MMA(1, 0, At, B0); PG8_MMA(1, 1, At, B1); } PG8_BAR; PG8_SCHED;
;         }
	s_add_i32 s44, s58, s5
	v_lshl_add_u64 v[216:217], v[216:217], 0, s[22:23]
	s_mov_b32 m0, s44
	ds_read_b128 v[184:187], v154 offset:49152
	ds_read_b128 v[188:191], v154 offset:50176
	ds_read_b128 v[192:195], v154 offset:51200
	ds_read_b128 v[196:199], v154 offset:52224
	ds_read_b128 v[200:203], v154 offset:53248
	ds_read_b128 v[204:207], v154 offset:54272
	ds_read_b128 v[208:211], v154 offset:55296
	ds_read_b128 v[212:215], v154 offset:56320
	global_load_lds_dwordx4 v[216:217], off
	s_add_i32 m0, s44, 0x2000
	s_add_u32 s42, s42, 0x80080
	v_lshl_add_u64 v[216:217], v[218:219], 0, s[22:23]
	s_addc_u32 s43, s43, 0
	s_add_i32 s44, s59, s5
	global_load_lds_dwordx4 v[216:217], off
	v_lshl_add_u64 v[216:217], s[42:43], 0, v[132:133]
	s_mov_b32 m0, s44
	s_nop 0
	global_load_lds_dwordx4 v[216:217], off
	v_lshl_add_u64 v[216:217], s[42:43], 0, v[136:137]
	s_add_i32 m0, s44, 0x2000
	s_nop 0
	global_load_lds_dwordx4 v[216:217], off
	v_lshl_add_u64 v[216:217], v[220:221], 0, s[22:23]
	s_mov_b32 m0, s46
	s_nop 0
	global_load_lds_dwordx4 v[216:217], off
	v_lshl_add_u64 v[216:217], v[222:223], 0, s[22:23]
	s_mov_b32 m0, s47
	s_nop 0
	global_load_lds_dwordx4 v[216:217], off
	s_waitcnt vmcnt(8)
	s_waitcnt lgkmcnt(0)
	s_barrier
	s_waitcnt lgkmcnt(0)
	v_mfma_f32_16x16x32_bf16 v[62:65], v[146:149], v[184:187], v[62:65]
	v_mfma_f32_16x16x32_bf16 v[58:61], v[160:163], v[184:187], v[58:61]
	v_mfma_f32_16x16x32_bf16 v[46:49], v[146:149], v[192:195], v[46:49]
	v_mfma_f32_16x16x32_bf16 v[42:45], v[160:163], v[192:195], v[42:45]
	v_mfma_f32_16x16x32_bf16 v[30:33], v[146:149], v[200:203], v[30:33]
	v_mfma_f32_16x16x32_bf16 v[26:29], v[160:163], v[200:203], v[26:29]
	v_mfma_f32_16x16x32_bf16 v[14:17], v[146:149], v[208:211], v[14:17]
	v_mfma_f32_16x16x32_bf16 v[10:13], v[160:163], v[208:211], v[10:13]
	v_mfma_f32_16x16x32_bf16 v[62:65], v[156:159], v[188:191], v[62:65]
	v_mfma_f32_16x16x32_bf16 v[58:61], v[164:167], v[188:191], v[58:61]
	v_mfma_f32_16x16x32_bf16 v[46:49], v[156:159], v[196:199], v[46:49]
	v_mfma_f32_16x16x32_bf16 v[42:45], v[164:167], v[196:199], v[42:45]
	v_mfma_f32_16x16x32_bf16 v[30:33], v[156:159], v[204:207], v[30:33]
	v_mfma_f32_16x16x32_bf16 v[26:29], v[164:167], v[204:207], v[26:29]
	v_mfma_f32_16x16x32_bf16 v[14:17], v[156:159], v[212:215], v[14:17]
	v_mfma_f32_16x16x32_bf16 v[10:13], v[164:167], v[212:215], v[10:13]
	v_mfma_f32_16x16x32_bf16 v[54:57], v[168:171], v[184:187], v[54:57]
	v_mfma_f32_16x16x32_bf16 v[50:53], v[176:179], v[184:187], v[50:53]
	v_mfma_f32_16x16x32_bf16 v[38:41], v[168:171], v[192:195], v[38:41]
	v_mfma_f32_16x16x32_bf16 v[34:37], v[176:179], v[192:195], v[34:37]
	v_mfma_f32_16x16x32_bf16 v[22:25], v[168:171], v[200:203], v[22:25]
	v_mfma_f32_16x16x32_bf16 v[18:21], v[176:179], v[200:203], v[18:21]
	v_mfma_f32_16x16x32_bf16 v[6:9], v[168:171], v[208:211], v[6:9]
	v_mfma_f32_16x16x32_bf16 v[2:5], v[176:179], v[208:211], v[2:5]
	v_mfma_f32_16x16x32_bf16 v[54:57], v[172:175], v[188:191], v[54:57]
	v_mfma_f32_16x16x32_bf16 v[50:53], v[180:183], v[188:191], v[50:53]
	v_mfma_f32_16x16x32_bf16 v[38:41], v[172:175], v[196:199], v[38:41]
	v_mfma_f32_16x16x32_bf16 v[34:37], v[180:183], v[196:199], v[34:37]
	v_mfma_f32_16x16x32_bf16 v[22:25], v[172:175], v[204:207], v[22:25]
	v_mfma_f32_16x16x32_bf16 v[18:21], v[180:183], v[204:207], v[18:21]
	v_mfma_f32_16x16x32_bf16 v[6:9], v[172:175], v[212:215], v[6:9]
	v_mfma_f32_16x16x32_bf16 v[2:5], v[180:183], v[212:215], v[2:5]
	s_barrier
	s_add_i32 s57, s57, 2
	s_add_u32 s40, s40, 0x100
	s_addc_u32 s41, s41, 0
	s_add_u32 s55, s55, 0x100
	s_addc_u32 s56, s56, 0
	s_cmp_gt_u32 s57, 29
	s_cbranch_scc0 .LBB0_830
	s_branch .Lpeel_exit_1

; #define PG8_BAR __builtin_amdgcn_s_barrier()
; template <class Epi, class Sched, bool GATHER, bool LIGHTSKIP = false>
; __device__ __forceinline__ void gemm_phase(LAS unsigned char* lds, LAS unsigned char* xl, const int lda, const int ldb, const int K, const Sched& S, const Epi& E) {
;     ...
;         }
;         if (wr == 0) PG8_BAR;
.Lpeel_exit_1:
	s_and_b64 vcc, exec, s[28:29]
	s_cbranch_vccz .LBB0_833
	s_barrier

; #define PG8_STAGE_B(b, h, bp) PG8_STAGE2(PG8_SB(b, h), (bp) + (h) * hstepB, voffB[0], voffB[1])
; #define PG8_STAGE_A(b, h, ap, NX) do { if constexpr (GATHER) { const unsigned _o0 = (NX) ? vn[h][0] : vc[h][0], _o1 = (NX) ? vn[h][1] : vc[h][1]; PG8_STAGE2(PG8_SA(b, h), (ap), _o0, _o1); } \
;         else { PG8_STAGE2(PG8_SA(b, h), (ap) + (h) * hstepA, voffA[0], voffA[1]); } } while (0)
; #define PG8_LDA(dst, b, h) do { _Pragma("unroll") for (int m = 0; m < 4; ++m) _Pragma("unroll") for (int k = 0; k < 2; ++k) dst[m][k] = *(const LAS bf16x8*)(lds + PG8_SA(b, h) + aoff + m * 2048 + k * 1024); } while (0)
; #define PG8_LDB(dst, b, h) do { _Pragma("unroll") for (int n = 0; n < 2; ++n) _Pragma("unroll") for (int k = 0; k < 2; ++k) dst[n][k] = *(const LAS bf16x8*)(lds + PG8_SB(b, h) + boff + n * 2048 + k * 1024); } while (0)
; #define PG8_MMA(ai, bj, At, Bt) do { __builtin_amdgcn_s_setprio(1); _Pragma("unroll") for (int m = 0; m < 4; ++m) _Pragma("unroll") for (int n = 0; n < 2; ++n) _Pragma("unroll") for (int k = 0; k < 2; ++k) \
;         acc[ai][bj][m][n] = __builtin_amdgcn_mfma_f32_16x16x32_bf16(Bt[n][k], At[m][k], acc[ai][bj][m][n], 0, 0, 0); __builtin_amdgcn_s_setprio(0); } while (0)
; #define PG8_WAIT_V(n) asm volatile("s_waitcnt vmcnt(" #n ")" ::: "memory")
; template <class Epi, class Sched, bool GATHER, bool LIGHTSKIP = false>
; __device__ __forceinline__ void gemm_phase(LAS unsigned char* lds, LAS unsigned char* xl, const int lda, const int ldb, const int K, const Sched& S, const Epi& E) {
;     ...
;     GUnit cur, nxt; int ui = 0;
;     if (!S.next(0, cur)) return;
;     Acc acc;
; #pragma unroll
;     for (int a = 0; a < 2; ++a)
; #pragma unroll
;         for (int b = 0; b < 2; ++b)
; #pragma unroll
;             for (int m = 0; m < 4; ++m)
; #pragma unroll
;                 for (int n = 0; n < 2; ++n) acc[a][b][m][n] = (f32x4){0.f, 0.f, 0.f, 0.f};
;     ...
;             PG8_LDB(B0, 0, 0); PG8_LDB(B1, 0, 1); PG8_SCHED; PG8_LDA(At, 0, 0); PG8_STAGE_A(1, 1, a1, false);
;             PG8_WAIT_V(8); PG8_WAIT_L(0); PG8_BAR; PG8_MMA(0, 0, At, B0); PG8_MMA(0, 1, At, B1); PG8_BAR; PG8_SCHED;
;             PG8_LDA(At, 0, 1); PG8_STAGE_B(0, 0, b2); PG8_STAGE_B(0, 1, b2); PG8_STAGE_A(0, 0, a2, last);
;             PG8_WAIT_V(8); PG8_WAIT_L(0); PG8_BAR; if (!light) { PG8_MMA(1, 0, At, B0); PG8_MMA(1, 1, At, B1); } PG8_BAR; PG8_SCHED;
.LBB0_937:
	s_add_u32 s62, s62, 0x80080
	s_addc_u32 s63, s63, 0
	s_add_u32 s84, s64, 0x100
	s_addc_u32 s85, s65, 0
	s_mov_b32 s86, -2
	ds_read_b128 v[98:101], v210
	ds_read_b128 v[102:105], v210 offset:1024
	ds_read_b128 v[106:109], v210 offset:2048
	ds_read_b128 v[110:113], v210 offset:3072
	ds_read_b128 v[118:121], v211
	ds_read_b128 v[122:125], v211 offset:1024
	ds_read_b128 v[126:129], v211 offset:2048
	ds_read_b128 v[130:133], v211 offset:3072
	s_add_u32 s64, s62, 0xfff80080
	s_addc_u32 s65, s63, -1
	s_cmp_eq_u32 s86, 28
	s_cselect_b32 s67, s55, s65
	s_cselect_b32 s66, s54, s64
	s_cselect_b32 s65, s57, s85
	s_cselect_b32 s64, s56, s84
	v_lshl_add_u64 v[230:231], s[62:63], 0, v[170:171]
	s_add_i32 m0, s5, 0xc000
	ds_read_b128 v[174:177], v212
	ds_read_b128 v[178:181], v212 offset:1024
	ds_read_b128 v[182:185], v212 offset:2048
	ds_read_b128 v[186:189], v212 offset:3072
	ds_read_b128 v[214:217], v212 offset:4096
	ds_read_b128 v[218:221], v212 offset:5120
	ds_read_b128 v[222:225], v212 offset:6144
	ds_read_b128 v[226:229], v212 offset:7168
	global_load_lds_dwordx4 v[230:231], off
	v_lshl_add_u64 v[230:231], s[62:63], 0, v[172:173]
	s_add_i32 m0, s5, 0xe000
	s_nop 0
	global_load_lds_dwordx4 v[230:231], off
	s_waitcnt vmcnt(8)
	s_waitcnt lgkmcnt(0)
	s_barrier
	s_waitcnt lgkmcnt(0)
	v_mfma_f32_16x16x32_bf16 v[158:161], v[98:101], v[174:177], 0
	v_mfma_f32_16x16x32_bf16 v[154:157], v[106:109], v[174:177], 0
	v_mfma_f32_16x16x32_bf16 v[142:145], v[98:101], v[182:185], 0
	v_mfma_f32_16x16x32_bf16 v[138:141], v[106:109], v[182:185], 0
	v_mfma_f32_16x16x32_bf16 v[94:97], v[98:101], v[214:217], 0
	v_mfma_f32_16x16x32_bf16 v[90:93], v[106:109], v[214:217], 0
	v_mfma_f32_16x16x32_bf16 v[78:81], v[98:101], v[222:225], 0
	v_mfma_f32_16x16x32_bf16 v[74:77], v[106:109], v[222:225], 0
	v_mfma_f32_16x16x32_bf16 v[158:161], v[102:105], v[178:181], v[158:161]
	v_mfma_f32_16x16x32_bf16 v[154:157], v[110:113], v[178:181], v[154:157]
	v_mfma_f32_16x16x32_bf16 v[142:145], v[102:105], v[186:189], v[142:145]
	v_mfma_f32_16x16x32_bf16 v[138:141], v[110:113], v[186:189], v[138:141]
	v_mfma_f32_16x16x32_bf16 v[94:97], v[102:105], v[218:221], v[94:97]
	v_mfma_f32_16x16x32_bf16 v[90:93], v[110:113], v[218:221], v[90:93]
	v_mfma_f32_16x16x32_bf16 v[78:81], v[102:105], v[226:229], v[78:81]
	v_mfma_f32_16x16x32_bf16 v[74:77], v[110:113], v[226:229], v[74:77]
	v_mfma_f32_16x16x32_bf16 v[150:153], v[118:121], v[174:177], 0
	v_mfma_f32_16x16x32_bf16 v[146:149], v[126:129], v[174:177], 0
	v_mfma_f32_16x16x32_bf16 v[134:137], v[118:121], v[182:185], 0
	v_mfma_f32_16x16x32_bf16 v[114:117], v[126:129], v[182:185], 0
	v_mfma_f32_16x16x32_bf16 v[86:89], v[118:121], v[214:217], 0
	v_mfma_f32_16x16x32_bf16 v[82:85], v[126:129], v[214:217], 0
	v_mfma_f32_16x16x32_bf16 v[70:73], v[118:121], v[222:225], 0
	v_mfma_f32_16x16x32_bf16 v[66:69], v[126:129], v[222:225], 0
	v_mfma_f32_16x16x32_bf16 v[150:153], v[122:125], v[178:181], v[150:153]
	v_mfma_f32_16x16x32_bf16 v[146:149], v[130:133], v[178:181], v[146:149]
	v_mfma_f32_16x16x32_bf16 v[134:137], v[122:125], v[186:189], v[134:137]
	v_mfma_f32_16x16x32_bf16 v[114:117], v[130:133], v[186:189], v[114:117]
	v_mfma_f32_16x16x32_bf16 v[86:89], v[122:125], v[218:221], v[86:89]
	v_mfma_f32_16x16x32_bf16 v[82:85], v[130:133], v[218:221], v[82:85]
	v_mfma_f32_16x16x32_bf16 v[70:73], v[122:125], v[226:229], v[70:73]
	v_mfma_f32_16x16x32_bf16 v[66:69], v[130:133], v[226:229], v[66:69]
	s_barrier
	s_add_i32 s87, s72, s4
	v_lshl_add_u64 v[230:231], s[64:65], 0, v[164:165]
	s_mov_b32 m0, s87
	ds_read_b128 v[174:177], v212 offset:16384
	ds_read_b128 v[178:181], v212 offset:17408
	ds_read_b128 v[182:185], v212 offset:18432
	ds_read_b128 v[186:189], v212 offset:19456
	ds_read_b128 v[214:217], v212 offset:20480
	ds_read_b128 v[218:221], v212 offset:21504
	ds_read_b128 v[222:225], v212 offset:22528
	ds_read_b128 v[226:229], v212 offset:23552
	global_load_lds_dwordx4 v[230:231], off
	s_add_i32 m0, s87, 0x2000
	s_add_u32 s88, s64, 0x80000
	v_lshl_add_u64 v[232:233], s[64:65], 0, v[168:169]
	s_addc_u32 s89, s65, 0
	s_add_i32 s87, s73, s4
	global_load_lds_dwordx4 v[232:233], off
	v_lshl_add_u64 v[234:235], s[88:89], 0, v[164:165]
	s_mov_b32 m0, s87
	v_lshl_add_u64 v[236:237], s[66:67], 0, v[166:167]
	global_load_lds_dwordx4 v[234:235], off
	v_lshl_add_u64 v[234:235], s[88:89], 0, v[168:169]
	s_add_i32 m0, s87, 0x2000
	s_nop 0
	global_load_lds_dwordx4 v[234:235], off
	v_lshl_add_u64 v[234:235], s[66:67], 0, v[162:163]
	s_mov_b32 m0, s5
	s_nop 0
	global_load_lds_dwordx4 v[234:235], off
	s_mov_b32 m0, s6
	s_nop 0
	global_load_lds_dwordx4 v[236:237], off
	s_waitcnt vmcnt(8)
	s_waitcnt lgkmcnt(0)
	s_barrier
; #define PG8_STAGE_A(b, h, ap, NX) do { if constexpr (GATHER) { const unsigned _o0 = (NX) ? vn[h][0] : vc[h][0], _o1 = (NX) ? vn[h][1] : vc[h][1]; PG8_STAGE2(PG8_SA(b, h), (ap), _o0, _o1); } \
;         else { PG8_STAGE2(PG8_SA(b, h), (ap) + (h) * hstepA, voffA[0], voffA[1]); } } while (0)
; #define PG8_LDA(dst, b, h) do { _Pragma("unroll") for (int m = 0; m < 4; ++m) _Pragma("unroll") for (int k = 0; k < 2; ++k) dst[m][k] = *(const LAS bf16x8*)(lds + PG8_SA(b, h) + aoff + m * 2048 + k * 1024); } while (0)
; #define PG8_LDB(dst, b, h) do { _Pragma("unroll") for (int n = 0; n < 2; ++n) _Pragma("unroll") for (int k = 0; k < 2; ++k) dst[n][k] = *(const LAS bf16x8*)(lds + PG8_SB(b, h) + boff + n * 2048 + k * 1024); } while (0)
; #define PG8_MMA(ai, bj, At, Bt) do { __builtin_amdgcn_s_setprio(1); _Pragma("unroll") for (int m = 0; m < 4; ++m) _Pragma("unroll") for (int n = 0; n < 2; ++n) _Pragma("unroll") for (int k = 0; k < 2; ++k) \
;         acc[ai][bj][m][n] = __builtin_amdgcn_mfma_f32_16x16x32_bf16(Bt[n][k], At[m][k], acc[ai][bj][m][n], 0, 0, 0); __builtin_amdgcn_s_setprio(0); } while (0)
; #define PG8_WAIT_V(n) asm volatile("s_waitcnt vmcnt(" #n ")" ::: "memory")
; #define PG8_WAIT_L(n) asm volatile("s_waitcnt lgkmcnt(" #n ")" ::: "memory")
; #define PG8_BAR __builtin_amdgcn_s_barrier()
; #define PG8_SCHED __builtin_amdgcn_sched_barrier(0)
; template <class Epi, class Sched, bool GATHER, bool LIGHTSKIP = false>
; __device__ __forceinline__ void gemm_phase(LAS unsigned char* lds, LAS unsigned char* xl, const int lda, const int ldb, const int K, const Sched& S, const Epi& E) {
;     ...
;             PG8_WAIT_V(8); PG8_WAIT_L(0); PG8_BAR; if (!light) { PG8_MMA(1, 0, At, B0); PG8_MMA(1, 1, At, B1); } PG8_BAR; PG8_SCHED;
;             PG8_LDB(B0, 1, 0); PG8_LDB(B1, 1, 1); PG8_SCHED; PG8_LDA(At, 1, 0); PG8_STAGE_A(0, 1, a2, last);
;             PG8_WAIT_V(8); PG8_WAIT_L(0); PG8_BAR; PG8_MMA(0, 0, At, B0); PG8_MMA(0, 1, At, B1); PG8_BAR; PG8_SCHED;
	s_waitcnt lgkmcnt(0)
	v_mfma_f32_16x16x32_bf16 v[62:65], v[98:101], v[174:177], 0
	v_mfma_f32_16x16x32_bf16 v[58:61], v[106:109], v[174:177], 0
	v_mfma_f32_16x16x32_bf16 v[46:49], v[98:101], v[182:185], 0
	v_mfma_f32_16x16x32_bf16 v[42:45], v[106:109], v[182:185], 0
	v_mfma_f32_16x16x32_bf16 v[30:33], v[98:101], v[214:217], 0
	v_mfma_f32_16x16x32_bf16 v[26:29], v[106:109], v[214:217], 0
	v_mfma_f32_16x16x32_bf16 v[14:17], v[98:101], v[222:225], 0
	v_mfma_f32_16x16x32_bf16 v[10:13], v[106:109], v[222:225], 0
	v_mfma_f32_16x16x32_bf16 v[62:65], v[102:105], v[178:181], v[62:65]
	v_mfma_f32_16x16x32_bf16 v[58:61], v[110:113], v[178:181], v[58:61]
	v_mfma_f32_16x16x32_bf16 v[46:49], v[102:105], v[186:189], v[46:49]
	v_mfma_f32_16x16x32_bf16 v[42:45], v[110:113], v[186:189], v[42:45]
	v_mfma_f32_16x16x32_bf16 v[30:33], v[102:105], v[218:221], v[30:33]
	v_mfma_f32_16x16x32_bf16 v[26:29], v[110:113], v[218:221], v[26:29]
	v_mfma_f32_16x16x32_bf16 v[14:17], v[102:105], v[226:229], v[14:17]
	v_mfma_f32_16x16x32_bf16 v[10:13], v[110:113], v[226:229], v[10:13]
	v_mfma_f32_16x16x32_bf16 v[54:57], v[118:121], v[174:177], 0
	v_mfma_f32_16x16x32_bf16 v[50:53], v[126:129], v[174:177], 0
	v_mfma_f32_16x16x32_bf16 v[38:41], v[118:121], v[182:185], 0
	v_mfma_f32_16x16x32_bf16 v[34:37], v[126:129], v[182:185], 0
	v_mfma_f32_16x16x32_bf16 v[22:25], v[118:121], v[214:217], 0
	v_mfma_f32_16x16x32_bf16 v[18:21], v[126:129], v[214:217], 0
	v_mfma_f32_16x16x32_bf16 v[6:9], v[118:121], v[222:225], 0
	v_mfma_f32_16x16x32_bf16 v[2:5], v[126:129], v[222:225], 0
	v_mfma_f32_16x16x32_bf16 v[54:57], v[122:125], v[178:181], v[54:57]
	v_mfma_f32_16x16x32_bf16 v[50:53], v[130:133], v[178:181], v[50:53]
	v_mfma_f32_16x16x32_bf16 v[38:41], v[122:125], v[186:189], v[38:41]
	v_mfma_f32_16x16x32_bf16 v[34:37], v[130:133], v[186:189], v[34:37]
	v_mfma_f32_16x16x32_bf16 v[22:25], v[122:125], v[218:221], v[22:25]
	v_mfma_f32_16x16x32_bf16 v[18:21], v[130:133], v[218:221], v[18:21]
	v_mfma_f32_16x16x32_bf16 v[6:9], v[122:125], v[226:229], v[6:9]
	v_mfma_f32_16x16x32_bf16 v[2:5], v[130:133], v[226:229], v[2:5]
	s_barrier
	s_add_i32 s87, 0, 0x18000
	s_add_i32 s88, 0, 0x1c000
	v_add_u32_e32 v110, s87, v190
	v_add_u32_e32 v130, s88, v190
	ds_read_b128 v[98:101], v110
	ds_read_b128 v[102:105], v110 offset:1024
	ds_read_b128 v[106:109], v110 offset:2048
	ds_read_b128 v[110:113], v110 offset:3072
	ds_read_b128 v[118:121], v130
	ds_read_b128 v[122:125], v130 offset:1024
	ds_read_b128 v[126:129], v130 offset:2048
	ds_read_b128 v[130:133], v130 offset:3072
	s_add_u32 s66, s66, 0x80000
	s_addc_u32 s67, s67, 0
	s_mov_b32 m0, s7
	v_lshl_add_u64 v[238:239], s[66:67], 0, v[162:163]
	ds_read_b128 v[174:177], v212 offset:32768
	ds_read_b128 v[178:181], v212 offset:33792
	ds_read_b128 v[182:185], v212 offset:34816
	ds_read_b128 v[186:189], v212 offset:35840
	ds_read_b128 v[214:217], v212 offset:36864
	ds_read_b128 v[218:221], v212 offset:37888
	ds_read_b128 v[222:225], v212 offset:38912
	ds_read_b128 v[226:229], v212 offset:39936
	global_load_lds_dwordx4 v[238:239], off
	v_lshl_add_u64 v[238:239], s[66:67], 0, v[166:167]
	s_mov_b32 m0, s26
	s_nop 0
	global_load_lds_dwordx4 v[238:239], off
	s_waitcnt vmcnt(8)
	s_waitcnt lgkmcnt(0)
	s_barrier
	s_waitcnt lgkmcnt(0)
	v_mfma_f32_16x16x32_bf16 v[158:161], v[98:101], v[174:177], v[158:161]
	v_mfma_f32_16x16x32_bf16 v[154:157], v[106:109], v[174:177], v[154:157]
	v_mfma_f32_16x16x32_bf16 v[142:145], v[98:101], v[182:185], v[142:145]
	v_mfma_f32_16x16x32_bf16 v[138:141], v[106:109], v[182:185], v[138:141]
	v_mfma_f32_16x16x32_bf16 v[94:97], v[98:101], v[214:217], v[94:97]
	v_mfma_f32_16x16x32_bf16 v[90:93], v[106:109], v[214:217], v[90:93]
	v_mfma_f32_16x16x32_bf16 v[78:81], v[98:101], v[222:225], v[78:81]
	v_mfma_f32_16x16x32_bf16 v[74:77], v[106:109], v[222:225], v[74:77]
	v_mfma_f32_16x16x32_bf16 v[158:161], v[102:105], v[178:181], v[158:161]
	v_mfma_f32_16x16x32_bf16 v[154:157], v[110:113], v[178:181], v[154:157]
	v_mfma_f32_16x16x32_bf16 v[142:145], v[102:105], v[186:189], v[142:145]
	v_mfma_f32_16x16x32_bf16 v[138:141], v[110:113], v[186:189], v[138:141]
	v_mfma_f32_16x16x32_bf16 v[94:97], v[102:105], v[218:221], v[94:97]
	v_mfma_f32_16x16x32_bf16 v[90:93], v[110:113], v[218:221], v[90:93]
	v_mfma_f32_16x16x32_bf16 v[78:81], v[102:105], v[226:229], v[78:81]
	v_mfma_f32_16x16x32_bf16 v[74:77], v[110:113], v[226:229], v[74:77]
	v_mfma_f32_16x16x32_bf16 v[150:153], v[118:121], v[174:177], v[150:153]
	v_mfma_f32_16x16x32_bf16 v[146:149], v[126:129], v[174:177], v[146:149]
	v_mfma_f32_16x16x32_bf16 v[134:137], v[118:121], v[182:185], v[134:137]
	v_mfma_f32_16x16x32_bf16 v[114:117], v[126:129], v[182:185], v[114:117]
	v_mfma_f32_16x16x32_bf16 v[86:89], v[118:121], v[214:217], v[86:89]
	v_mfma_f32_16x16x32_bf16 v[82:85], v[126:129], v[214:217], v[82:85]
	v_mfma_f32_16x16x32_bf16 v[70:73], v[118:121], v[222:225], v[70:73]
	v_mfma_f32_16x16x32_bf16 v[66:69], v[126:129], v[222:225], v[66:69]
	v_mfma_f32_16x16x32_bf16 v[150:153], v[122:125], v[178:181], v[150:153]
	v_mfma_f32_16x16x32_bf16 v[146:149], v[130:133], v[178:181], v[146:149]
	v_mfma_f32_16x16x32_bf16 v[134:137], v[122:125], v[186:189], v[134:137]
	v_mfma_f32_16x16x32_bf16 v[114:117], v[130:133], v[186:189], v[114:117]
	v_mfma_f32_16x16x32_bf16 v[86:89], v[122:125], v[218:221], v[86:89]
	v_mfma_f32_16x16x32_bf16 v[82:85], v[130:133], v[218:221], v[82:85]
	v_mfma_f32_16x16x32_bf16 v[70:73], v[122:125], v[226:229], v[70:73]
	v_mfma_f32_16x16x32_bf16 v[66:69], v[130:133], v[226:229], v[66:69]
	s_barrier
; #define PG8_STAGE_B(b, h, bp) PG8_STAGE2(PG8_SB(b, h), (bp) + (h) * hstepB, voffB[0], voffB[1])
; #define PG8_STAGE_A(b, h, ap, NX) do { if constexpr (GATHER) { const unsigned _o0 = (NX) ? vn[h][0] : vc[h][0], _o1 = (NX) ? vn[h][1] : vc[h][1]; PG8_STAGE2(PG8_SA(b, h), (ap), _o0, _o1); } \
;         else { PG8_STAGE2(PG8_SA(b, h), (ap) + (h) * hstepA, voffA[0], voffA[1]); } } while (0)
; #define PG8_LDA(dst, b, h) do { _Pragma("unroll") for (int m = 0; m < 4; ++m) _Pragma("unroll") for (int k = 0; k < 2; ++k) dst[m][k] = *(const LAS bf16x8*)(lds + PG8_SA(b, h) + aoff + m * 2048 + k * 1024); } while (0)
; #define PG8_MMA(ai, bj, At, Bt) do { __builtin_amdgcn_s_setprio(1); _Pragma("unroll") for (int m = 0; m < 4; ++m) _Pragma("unroll") for (int n = 0; n < 2; ++n) _Pragma("unroll") for (int k = 0; k < 2; ++k) \
;         acc[ai][bj][m][n] = __builtin_amdgcn_mfma_f32_16x16x32_bf16(Bt[n][k], At[m][k], acc[ai][bj][m][n], 0, 0, 0); __builtin_amdgcn_s_setprio(0); } while (0)
; #define PG8_WAIT_V(n) asm volatile("s_waitcnt vmcnt(" #n ")" ::: "memory")
; #define PG8_WAIT_L(n) asm volatile("s_waitcnt lgkmcnt(" #n ")" ::: "memory")
; #define PG8_BAR __builtin_amdgcn_s_barrier()
; #define PG8_SCHED __builtin_amdgcn_sched_barrier(0)
; template <class Epi, class Sched, bool GATHER, bool LIGHTSKIP = false>
; __device__ __forceinline__ void gemm_phase(LAS unsigned char* lds, LAS unsigned char* xl, const int lda, const int ldb, const int K, const Sched& S, const Epi& E) {
;     ...
;             PG8_LDA(At, 1, 1); PG8_STAGE_B(1, 0, b3); PG8_STAGE_B(1, 1, b3); PG8_STAGE_A(1, 0, a3, last);
;             PG8_WAIT_V(8); PG8_WAIT_L(0); PG8_BAR; if (!light) { PG8_MMA(1, 0, At, B0); PG8_MMA(1, 1, At, B1); } PG8_BAR; PG8_SCHED;
;         }
	s_add_i32 s66, s87, s4
	v_lshl_add_u64 v[230:231], v[230:231], 0, s[30:31]
	s_mov_b32 m0, s66
	ds_read_b128 v[174:177], v212 offset:49152
	ds_read_b128 v[178:181], v212 offset:50176
	ds_read_b128 v[182:185], v212 offset:51200
	ds_read_b128 v[186:189], v212 offset:52224
	ds_read_b128 v[214:217], v212 offset:53248
	ds_read_b128 v[218:221], v212 offset:54272
	ds_read_b128 v[222:225], v212 offset:55296
	ds_read_b128 v[226:229], v212 offset:56320
	global_load_lds_dwordx4 v[230:231], off
	s_add_i32 m0, s66, 0x2000
	s_add_u32 s64, s64, 0x80080
	v_lshl_add_u64 v[230:231], v[232:233], 0, s[30:31]
	s_addc_u32 s65, s65, 0
	s_add_i32 s66, s88, s4
	global_load_lds_dwordx4 v[230:231], off
	v_lshl_add_u64 v[230:231], s[64:65], 0, v[164:165]
	s_mov_b32 m0, s66
	s_nop 0
	global_load_lds_dwordx4 v[230:231], off
	v_lshl_add_u64 v[230:231], s[64:65], 0, v[168:169]
	s_add_i32 m0, s66, 0x2000
	s_nop 0
	global_load_lds_dwordx4 v[230:231], off
	v_lshl_add_u64 v[230:231], v[234:235], 0, s[30:31]
	s_mov_b32 m0, s69
	s_nop 0
	global_load_lds_dwordx4 v[230:231], off
	v_lshl_add_u64 v[230:231], v[236:237], 0, s[30:31]
	s_mov_b32 m0, s70
	s_nop 0
	global_load_lds_dwordx4 v[230:231], off
	s_waitcnt vmcnt(8)
	s_waitcnt lgkmcnt(0)
	s_barrier
	s_waitcnt lgkmcnt(0)
	v_mfma_f32_16x16x32_bf16 v[62:65], v[98:101], v[174:177], v[62:65]
	v_mfma_f32_16x16x32_bf16 v[58:61], v[106:109], v[174:177], v[58:61]
	v_mfma_f32_16x16x32_bf16 v[46:49], v[98:101], v[182:185], v[46:49]
	v_mfma_f32_16x16x32_bf16 v[42:45], v[106:109], v[182:185], v[42:45]
	v_mfma_f32_16x16x32_bf16 v[30:33], v[98:101], v[214:217], v[30:33]
	v_mfma_f32_16x16x32_bf16 v[26:29], v[106:109], v[214:217], v[26:29]
	v_mfma_f32_16x16x32_bf16 v[14:17], v[98:101], v[222:225], v[14:17]
	v_mfma_f32_16x16x32_bf16 v[10:13], v[106:109], v[222:225], v[10:13]
	v_mfma_f32_16x16x32_bf16 v[62:65], v[102:105], v[178:181], v[62:65]
	v_mfma_f32_16x16x32_bf16 v[58:61], v[110:113], v[178:181], v[58:61]
	v_mfma_f32_16x16x32_bf16 v[46:49], v[102:105], v[186:189], v[46:49]
	v_mfma_f32_16x16x32_bf16 v[42:45], v[110:113], v[186:189], v[42:45]
	v_mfma_f32_16x16x32_bf16 v[30:33], v[102:105], v[218:221], v[30:33]
	v_mfma_f32_16x16x32_bf16 v[26:29], v[110:113], v[218:221], v[26:29]
	v_mfma_f32_16x16x32_bf16 v[14:17], v[102:105], v[226:229], v[14:17]
	v_mfma_f32_16x16x32_bf16 v[10:13], v[110:113], v[226:229], v[10:13]
	v_mfma_f32_16x16x32_bf16 v[54:57], v[118:121], v[174:177], v[54:57]
	v_mfma_f32_16x16x32_bf16 v[50:53], v[126:129], v[174:177], v[50:53]
	v_mfma_f32_16x16x32_bf16 v[38:41], v[118:121], v[182:185], v[38:41]
	v_mfma_f32_16x16x32_bf16 v[34:37], v[126:129], v[182:185], v[34:37]
	v_mfma_f32_16x16x32_bf16 v[22:25], v[118:121], v[214:217], v[22:25]
	v_mfma_f32_16x16x32_bf16 v[18:21], v[126:129], v[214:217], v[18:21]
	v_mfma_f32_16x16x32_bf16 v[6:9], v[118:121], v[222:225], v[6:9]
	v_mfma_f32_16x16x32_bf16 v[2:5], v[126:129], v[222:225], v[2:5]
	v_mfma_f32_16x16x32_bf16 v[54:57], v[122:125], v[178:181], v[54:57]
	v_mfma_f32_16x16x32_bf16 v[50:53], v[130:133], v[178:181], v[50:53]
	v_mfma_f32_16x16x32_bf16 v[38:41], v[122:125], v[186:189], v[38:41]
	v_mfma_f32_16x16x32_bf16 v[34:37], v[130:133], v[186:189], v[34:37]
	v_mfma_f32_16x16x32_bf16 v[22:25], v[122:125], v[218:221], v[22:25]
	v_mfma_f32_16x16x32_bf16 v[18:21], v[130:133], v[218:221], v[18:21]
	v_mfma_f32_16x16x32_bf16 v[6:9], v[122:125], v[226:229], v[6:9]
	v_mfma_f32_16x16x32_bf16 v[2:5], v[130:133], v[226:229], v[2:5]
	s_barrier
	s_add_i32 s86, s86, 2
	s_add_u32 s62, s62, 0x100
	s_addc_u32 s63, s63, 0
	s_add_u32 s84, s84, 0x100
	s_addc_u32 s85, s85, 0
	s_cmp_gt_u32 s86, 29
	s_cbranch_scc0 .LBB0_938
	s_branch .Lpeel_exit_2

; #define PG8_BAR __builtin_amdgcn_s_barrier()
; template <class Epi, class Sched, bool GATHER, bool LIGHTSKIP = false>
; __device__ __forceinline__ void gemm_phase(LAS unsigned char* lds, LAS unsigned char* xl, const int lda, const int ldb, const int K, const Sched& S, const Epi& E) {
;     ...
;         }
;         if (wr == 0) PG8_BAR;
.Lpeel_exit_2:
	s_and_b64 vcc, exec, s[34:35]
	s_cbranch_vccz .LBB0_941
	s_barrier

; #define PG8_STAGE_B(b, h, bp) PG8_STAGE2(PG8_SB(b, h), (bp) + (h) * hstepB, voffB[0], voffB[1])
; #define PG8_STAGE_A(b, h, ap, NX) do { if constexpr (GATHER) { const unsigned _o0 = (NX) ? vn[h][0] : vc[h][0], _o1 = (NX) ? vn[h][1] : vc[h][1]; PG8_STAGE2(PG8_SA(b, h), (ap), _o0, _o1); } \
;         else { PG8_STAGE2(PG8_SA(b, h), (ap) + (h) * hstepA, voffA[0], voffA[1]); } } while (0)
; #define PG8_LDA(dst, b, h) do { _Pragma("unroll") for (int m = 0; m < 4; ++m) _Pragma("unroll") for (int k = 0; k < 2; ++k) dst[m][k] = *(const LAS bf16x8*)(lds + PG8_SA(b, h) + aoff + m * 2048 + k * 1024); } while (0)
; #define PG8_LDB(dst, b, h) do { _Pragma("unroll") for (int n = 0; n < 2; ++n) _Pragma("unroll") for (int k = 0; k < 2; ++k) dst[n][k] = *(const LAS bf16x8*)(lds + PG8_SB(b, h) + boff + n * 2048 + k * 1024); } while (0)
; #define PG8_MMA(ai, bj, At, Bt) do { __builtin_amdgcn_s_setprio(1); _Pragma("unroll") for (int m = 0; m < 4; ++m) _Pragma("unroll") for (int n = 0; n < 2; ++n) _Pragma("unroll") for (int k = 0; k < 2; ++k) \
;         acc[ai][bj][m][n] = __builtin_amdgcn_mfma_f32_16x16x32_bf16(Bt[n][k], At[m][k], acc[ai][bj][m][n], 0, 0, 0); __builtin_amdgcn_s_setprio(0); } while (0)
; #define PG8_WAIT_V(n) asm volatile("s_waitcnt vmcnt(" #n ")" ::: "memory")
; template <class Epi, class Sched, bool GATHER, bool LIGHTSKIP = false>
; __device__ __forceinline__ void gemm_phase(LAS unsigned char* lds, LAS unsigned char* xl, const int lda, const int ldb, const int K, const Sched& S, const Epi& E) {
;     ...
;     GUnit cur, nxt; int ui = 0;
;     if (!S.next(0, cur)) return;
;     Acc acc;
; #pragma unroll
;     for (int a = 0; a < 2; ++a)
; #pragma unroll
;         for (int b = 0; b < 2; ++b)
; #pragma unroll
;             for (int m = 0; m < 4; ++m)
; #pragma unroll
;                 for (int n = 0; n < 2; ++n) acc[a][b][m][n] = (f32x4){0.f, 0.f, 0.f, 0.f};
;     ...
;             PG8_LDB(B0, 0, 0); PG8_LDB(B1, 0, 1); PG8_SCHED; PG8_LDA(At, 0, 0); PG8_STAGE_A(1, 1, a1, false);
;             PG8_WAIT_V(8); PG8_WAIT_L(0); PG8_BAR; PG8_MMA(0, 0, At, B0); PG8_MMA(0, 1, At, B1); PG8_BAR; PG8_SCHED;
;             PG8_LDA(At, 0, 1); PG8_STAGE_B(0, 0, b2); PG8_STAGE_B(0, 1, b2); PG8_STAGE_A(0, 0, a2, last);
;             PG8_WAIT_V(8); PG8_WAIT_L(0); PG8_BAR; if (!light) { PG8_MMA(1, 0, At, B0); PG8_MMA(1, 1, At, B1); } PG8_BAR; PG8_SCHED;
.LBB0_1026:
	s_add_u32 s42, s42, 0x40080
	s_addc_u32 s43, s43, 0
	s_add_u32 s59, s44, 0x100
	s_addc_u32 s60, s45, 0
	s_mov_b32 s61, -2
	ds_read_b128 v[146:149], v184
	ds_read_b128 v[150:153], v184 offset:1024
	ds_read_b128 v[154:157], v184 offset:2048
	ds_read_b128 v[158:161], v184 offset:3072
	ds_read_b128 v[162:165], v185
	ds_read_b128 v[166:169], v185 offset:1024
	ds_read_b128 v[170:173], v185 offset:2048
	ds_read_b128 v[174:177], v185 offset:3072
	s_add_u32 s44, s42, 0xfffc0080
	s_addc_u32 s45, s43, -1
	s_cmp_eq_u32 s61, 12
	s_cselect_b32 s47, s39, s45
	s_cselect_b32 s46, s38, s44
	s_cselect_b32 s45, s41, s60
	s_cselect_b32 s44, s40, s59
	v_lshl_add_u64 v[216:217], s[42:43], 0, v[138:139]
	s_add_i32 m0, s6, 0xc000
	ds_read_b128 v[178:181], v186
	ds_read_b128 v[188:191], v186 offset:1024
	ds_read_b128 v[192:195], v186 offset:2048
	ds_read_b128 v[196:199], v186 offset:3072
	ds_read_b128 v[200:203], v186 offset:4096
	ds_read_b128 v[204:207], v186 offset:5120
	ds_read_b128 v[208:211], v186 offset:6144
	ds_read_b128 v[212:215], v186 offset:7168
	global_load_lds_dwordx4 v[216:217], off
	v_lshl_add_u64 v[216:217], s[42:43], 0, v[140:141]
	s_add_i32 m0, s6, 0xe000
	s_nop 0
	global_load_lds_dwordx4 v[216:217], off
	s_waitcnt vmcnt(8)
	s_waitcnt lgkmcnt(0)
	s_barrier
	s_waitcnt lgkmcnt(0)
	v_mfma_f32_16x16x32_bf16 v[126:129], v[146:149], v[178:181], 0
	v_mfma_f32_16x16x32_bf16 v[122:125], v[154:157], v[178:181], 0
	v_mfma_f32_16x16x32_bf16 v[110:113], v[146:149], v[192:195], 0
	v_mfma_f32_16x16x32_bf16 v[106:109], v[154:157], v[192:195], 0
	v_mfma_f32_16x16x32_bf16 v[94:97], v[146:149], v[200:203], 0
	v_mfma_f32_16x16x32_bf16 v[90:93], v[154:157], v[200:203], 0
	v_mfma_f32_16x16x32_bf16 v[78:81], v[146:149], v[208:211], 0
	v_mfma_f32_16x16x32_bf16 v[74:77], v[154:157], v[208:211], 0
	v_mfma_f32_16x16x32_bf16 v[126:129], v[150:153], v[188:191], v[126:129]
	v_mfma_f32_16x16x32_bf16 v[122:125], v[158:161], v[188:191], v[122:125]
	v_mfma_f32_16x16x32_bf16 v[110:113], v[150:153], v[196:199], v[110:113]
	v_mfma_f32_16x16x32_bf16 v[106:109], v[158:161], v[196:199], v[106:109]
	v_mfma_f32_16x16x32_bf16 v[94:97], v[150:153], v[204:207], v[94:97]
	v_mfma_f32_16x16x32_bf16 v[90:93], v[158:161], v[204:207], v[90:93]
	v_mfma_f32_16x16x32_bf16 v[78:81], v[150:153], v[212:215], v[78:81]
	v_mfma_f32_16x16x32_bf16 v[74:77], v[158:161], v[212:215], v[74:77]
	v_mfma_f32_16x16x32_bf16 v[118:121], v[162:165], v[178:181], 0
	v_mfma_f32_16x16x32_bf16 v[114:117], v[170:173], v[178:181], 0
	v_mfma_f32_16x16x32_bf16 v[102:105], v[162:165], v[192:195], 0
	v_mfma_f32_16x16x32_bf16 v[98:101], v[170:173], v[192:195], 0
	v_mfma_f32_16x16x32_bf16 v[86:89], v[162:165], v[200:203], 0
	v_mfma_f32_16x16x32_bf16 v[82:85], v[170:173], v[200:203], 0
	v_mfma_f32_16x16x32_bf16 v[70:73], v[162:165], v[208:211], 0
	v_mfma_f32_16x16x32_bf16 v[66:69], v[170:173], v[208:211], 0
	v_mfma_f32_16x16x32_bf16 v[118:121], v[166:169], v[188:191], v[118:121]
	v_mfma_f32_16x16x32_bf16 v[114:117], v[174:177], v[188:191], v[114:117]
	v_mfma_f32_16x16x32_bf16 v[102:105], v[166:169], v[196:199], v[102:105]
	v_mfma_f32_16x16x32_bf16 v[98:101], v[174:177], v[196:199], v[98:101]
	v_mfma_f32_16x16x32_bf16 v[86:89], v[166:169], v[204:207], v[86:89]
	v_mfma_f32_16x16x32_bf16 v[82:85], v[174:177], v[204:207], v[82:85]
	v_mfma_f32_16x16x32_bf16 v[70:73], v[166:169], v[212:215], v[70:73]
	v_mfma_f32_16x16x32_bf16 v[66:69], v[174:177], v[212:215], v[66:69]
	s_barrier
	s_add_i32 s62, s52, s5
	v_lshl_add_u64 v[216:217], s[44:45], 0, v[132:133]
	s_mov_b32 m0, s62
	ds_read_b128 v[178:181], v186 offset:16384
	ds_read_b128 v[188:191], v186 offset:17408
	ds_read_b128 v[192:195], v186 offset:18432
	ds_read_b128 v[196:199], v186 offset:19456
	ds_read_b128 v[200:203], v186 offset:20480
	ds_read_b128 v[204:207], v186 offset:21504
	ds_read_b128 v[208:211], v186 offset:22528
	ds_read_b128 v[212:215], v186 offset:23552
	global_load_lds_dwordx4 v[216:217], off
	s_add_i32 m0, s62, 0x2000
	s_add_u32 s62, s44, 0x40000
	v_lshl_add_u64 v[218:219], s[44:45], 0, v[136:137]
	s_addc_u32 s63, s45, 0
	s_add_i32 s64, s53, s5
	global_load_lds_dwordx4 v[218:219], off
	v_lshl_add_u64 v[220:221], s[62:63], 0, v[132:133]
	s_mov_b32 m0, s64
	v_lshl_add_u64 v[222:223], s[46:47], 0, v[134:135]
	global_load_lds_dwordx4 v[220:221], off
	v_lshl_add_u64 v[220:221], s[62:63], 0, v[136:137]
	s_add_i32 m0, s64, 0x2000
	s_nop 0
	global_load_lds_dwordx4 v[220:221], off
	v_lshl_add_u64 v[220:221], s[46:47], 0, v[130:131]
	s_mov_b32 m0, s6
	s_nop 0
	global_load_lds_dwordx4 v[220:221], off
	s_mov_b32 m0, s7
	s_nop 0
	global_load_lds_dwordx4 v[222:223], off
	s_waitcnt vmcnt(8)
	s_waitcnt lgkmcnt(0)
	s_barrier
; #define PG8_STAGE_A(b, h, ap, NX) do { if constexpr (GATHER) { const unsigned _o0 = (NX) ? vn[h][0] : vc[h][0], _o1 = (NX) ? vn[h][1] : vc[h][1]; PG8_STAGE2(PG8_SA(b, h), (ap), _o0, _o1); } \
;         else { PG8_STAGE2(PG8_SA(b, h), (ap) + (h) * hstepA, voffA[0], voffA[1]); } } while (0)
; #define PG8_LDA(dst, b, h) do { _Pragma("unroll") for (int m = 0; m < 4; ++m) _Pragma("unroll") for (int k = 0; k < 2; ++k) dst[m][k] = *(const LAS bf16x8*)(lds + PG8_SA(b, h) + aoff + m * 2048 + k * 1024); } while (0)
; #define PG8_LDB(dst, b, h) do { _Pragma("unroll") for (int n = 0; n < 2; ++n) _Pragma("unroll") for (int k = 0; k < 2; ++k) dst[n][k] = *(const LAS bf16x8*)(lds + PG8_SB(b, h) + boff + n * 2048 + k * 1024); } while (0)
; #define PG8_MMA(ai, bj, At, Bt) do { __builtin_amdgcn_s_setprio(1); _Pragma("unroll") for (int m = 0; m < 4; ++m) _Pragma("unroll") for (int n = 0; n < 2; ++n) _Pragma("unroll") for (int k = 0; k < 2; ++k) \
;         acc[ai][bj][m][n] = __builtin_amdgcn_mfma_f32_16x16x32_bf16(Bt[n][k], At[m][k], acc[ai][bj][m][n], 0, 0, 0); __builtin_amdgcn_s_setprio(0); } while (0)
; #define PG8_WAIT_V(n) asm volatile("s_waitcnt vmcnt(" #n ")" ::: "memory")
; #define PG8_WAIT_L(n) asm volatile("s_waitcnt lgkmcnt(" #n ")" ::: "memory")
; #define PG8_BAR __builtin_amdgcn_s_barrier()
; #define PG8_SCHED __builtin_amdgcn_sched_barrier(0)
; template <class Epi, class Sched, bool GATHER, bool LIGHTSKIP = false>
; __device__ __forceinline__ void gemm_phase(LAS unsigned char* lds, LAS unsigned char* xl, const int lda, const int ldb, const int K, const Sched& S, const Epi& E) {
;     ...
;             PG8_WAIT_V(8); PG8_WAIT_L(0); PG8_BAR; if (!light) { PG8_MMA(1, 0, At, B0); PG8_MMA(1, 1, At, B1); } PG8_BAR; PG8_SCHED;
;             PG8_LDB(B0, 1, 0); PG8_LDB(B1, 1, 1); PG8_SCHED; PG8_LDA(At, 1, 0); PG8_STAGE_A(0, 1, a2, last);
;             PG8_WAIT_V(8); PG8_WAIT_L(0); PG8_BAR; PG8_MMA(0, 0, At, B0); PG8_MMA(0, 1, At, B1); PG8_BAR; PG8_SCHED;
	s_waitcnt lgkmcnt(0)
	v_mfma_f32_16x16x32_bf16 v[62:65], v[146:149], v[178:181], 0
	v_mfma_f32_16x16x32_bf16 v[58:61], v[154:157], v[178:181], 0
	v_mfma_f32_16x16x32_bf16 v[46:49], v[146:149], v[192:195], 0
	v_mfma_f32_16x16x32_bf16 v[42:45], v[154:157], v[192:195], 0
	v_mfma_f32_16x16x32_bf16 v[30:33], v[146:149], v[200:203], 0
	v_mfma_f32_16x16x32_bf16 v[26:29], v[154:157], v[200:203], 0
	v_mfma_f32_16x16x32_bf16 v[14:17], v[146:149], v[208:211], 0
	v_mfma_f32_16x16x32_bf16 v[10:13], v[154:157], v[208:211], 0
	v_mfma_f32_16x16x32_bf16 v[62:65], v[150:153], v[188:191], v[62:65]
	v_mfma_f32_16x16x32_bf16 v[58:61], v[158:161], v[188:191], v[58:61]
	v_mfma_f32_16x16x32_bf16 v[46:49], v[150:153], v[196:199], v[46:49]
	v_mfma_f32_16x16x32_bf16 v[42:45], v[158:161], v[196:199], v[42:45]
	v_mfma_f32_16x16x32_bf16 v[30:33], v[150:153], v[204:207], v[30:33]
	v_mfma_f32_16x16x32_bf16 v[26:29], v[158:161], v[204:207], v[26:29]
	v_mfma_f32_16x16x32_bf16 v[14:17], v[150:153], v[212:215], v[14:17]
	v_mfma_f32_16x16x32_bf16 v[10:13], v[158:161], v[212:215], v[10:13]
	v_mfma_f32_16x16x32_bf16 v[54:57], v[162:165], v[178:181], 0
	v_mfma_f32_16x16x32_bf16 v[50:53], v[170:173], v[178:181], 0
	v_mfma_f32_16x16x32_bf16 v[38:41], v[162:165], v[192:195], 0
	v_mfma_f32_16x16x32_bf16 v[34:37], v[170:173], v[192:195], 0
	v_mfma_f32_16x16x32_bf16 v[22:25], v[162:165], v[200:203], 0
	v_mfma_f32_16x16x32_bf16 v[18:21], v[170:173], v[200:203], 0
	v_mfma_f32_16x16x32_bf16 v[6:9], v[162:165], v[208:211], 0
	v_mfma_f32_16x16x32_bf16 v[2:5], v[170:173], v[208:211], 0
	v_mfma_f32_16x16x32_bf16 v[54:57], v[166:169], v[188:191], v[54:57]
	v_mfma_f32_16x16x32_bf16 v[50:53], v[174:177], v[188:191], v[50:53]
	v_mfma_f32_16x16x32_bf16 v[38:41], v[166:169], v[196:199], v[38:41]
	v_mfma_f32_16x16x32_bf16 v[34:37], v[174:177], v[196:199], v[34:37]
	v_mfma_f32_16x16x32_bf16 v[22:25], v[166:169], v[204:207], v[22:25]
	v_mfma_f32_16x16x32_bf16 v[18:21], v[174:177], v[204:207], v[18:21]
	v_mfma_f32_16x16x32_bf16 v[6:9], v[166:169], v[212:215], v[6:9]
	v_mfma_f32_16x16x32_bf16 v[2:5], v[174:177], v[212:215], v[2:5]
	s_barrier
	s_add_i32 s62, 0, 0x18000
	s_add_i32 s63, 0, 0x1c000
	v_add_u32_e32 v158, s62, v182
	v_add_u32_e32 v174, s63, v182
	ds_read_b128 v[146:149], v158
	ds_read_b128 v[150:153], v158 offset:1024
	ds_read_b128 v[154:157], v158 offset:2048
	ds_read_b128 v[158:161], v158 offset:3072
	ds_read_b128 v[162:165], v174
	ds_read_b128 v[166:169], v174 offset:1024
	ds_read_b128 v[170:173], v174 offset:2048
	ds_read_b128 v[174:177], v174 offset:3072
	s_add_u32 s46, s46, 0x40000
	s_addc_u32 s47, s47, 0
	s_mov_b32 m0, s26
	v_lshl_add_u64 v[224:225], s[46:47], 0, v[130:131]
	ds_read_b128 v[178:181], v186 offset:32768
	ds_read_b128 v[188:191], v186 offset:33792
	ds_read_b128 v[192:195], v186 offset:34816
	ds_read_b128 v[196:199], v186 offset:35840
	ds_read_b128 v[200:203], v186 offset:36864
	ds_read_b128 v[204:207], v186 offset:37888
	ds_read_b128 v[208:211], v186 offset:38912
	ds_read_b128 v[212:215], v186 offset:39936
	global_load_lds_dwordx4 v[224:225], off
	v_lshl_add_u64 v[224:225], s[46:47], 0, v[134:135]
	s_mov_b32 m0, s27
	s_nop 0
	global_load_lds_dwordx4 v[224:225], off
	s_waitcnt vmcnt(8)
	s_waitcnt lgkmcnt(0)
	s_barrier
	s_waitcnt lgkmcnt(0)
	v_mfma_f32_16x16x32_bf16 v[126:129], v[146:149], v[178:181], v[126:129]
	v_mfma_f32_16x16x32_bf16 v[122:125], v[154:157], v[178:181], v[122:125]
	v_mfma_f32_16x16x32_bf16 v[110:113], v[146:149], v[192:195], v[110:113]
	v_mfma_f32_16x16x32_bf16 v[106:109], v[154:157], v[192:195], v[106:109]
	v_mfma_f32_16x16x32_bf16 v[94:97], v[146:149], v[200:203], v[94:97]
	v_mfma_f32_16x16x32_bf16 v[90:93], v[154:157], v[200:203], v[90:93]
	v_mfma_f32_16x16x32_bf16 v[78:81], v[146:149], v[208:211], v[78:81]
	v_mfma_f32_16x16x32_bf16 v[74:77], v[154:157], v[208:211], v[74:77]
	v_mfma_f32_16x16x32_bf16 v[126:129], v[150:153], v[188:191], v[126:129]
	v_mfma_f32_16x16x32_bf16 v[122:125], v[158:161], v[188:191], v[122:125]
	v_mfma_f32_16x16x32_bf16 v[110:113], v[150:153], v[196:199], v[110:113]
	v_mfma_f32_16x16x32_bf16 v[106:109], v[158:161], v[196:199], v[106:109]
	v_mfma_f32_16x16x32_bf16 v[94:97], v[150:153], v[204:207], v[94:97]
	v_mfma_f32_16x16x32_bf16 v[90:93], v[158:161], v[204:207], v[90:93]
	v_mfma_f32_16x16x32_bf16 v[78:81], v[150:153], v[212:215], v[78:81]
	v_mfma_f32_16x16x32_bf16 v[74:77], v[158:161], v[212:215], v[74:77]
	v_mfma_f32_16x16x32_bf16 v[118:121], v[162:165], v[178:181], v[118:121]
	v_mfma_f32_16x16x32_bf16 v[114:117], v[170:173], v[178:181], v[114:117]
	v_mfma_f32_16x16x32_bf16 v[102:105], v[162:165], v[192:195], v[102:105]
	v_mfma_f32_16x16x32_bf16 v[98:101], v[170:173], v[192:195], v[98:101]
	v_mfma_f32_16x16x32_bf16 v[86:89], v[162:165], v[200:203], v[86:89]
	v_mfma_f32_16x16x32_bf16 v[82:85], v[170:173], v[200:203], v[82:85]
	v_mfma_f32_16x16x32_bf16 v[70:73], v[162:165], v[208:211], v[70:73]
	v_mfma_f32_16x16x32_bf16 v[66:69], v[170:173], v[208:211], v[66:69]
	v_mfma_f32_16x16x32_bf16 v[118:121], v[166:169], v[188:191], v[118:121]
	v_mfma_f32_16x16x32_bf16 v[114:117], v[174:177], v[188:191], v[114:117]
	v_mfma_f32_16x16x32_bf16 v[102:105], v[166:169], v[196:199], v[102:105]
	v_mfma_f32_16x16x32_bf16 v[98:101], v[174:177], v[196:199], v[98:101]
	v_mfma_f32_16x16x32_bf16 v[86:89], v[166:169], v[204:207], v[86:89]
	v_mfma_f32_16x16x32_bf16 v[82:85], v[174:177], v[204:207], v[82:85]
	v_mfma_f32_16x16x32_bf16 v[70:73], v[166:169], v[212:215], v[70:73]
	v_mfma_f32_16x16x32_bf16 v[66:69], v[174:177], v[212:215], v[66:69]
	s_barrier
; #define PG8_STAGE_B(b, h, bp) PG8_STAGE2(PG8_SB(b, h), (bp) + (h) * hstepB, voffB[0], voffB[1])
; #define PG8_STAGE_A(b, h, ap, NX) do { if constexpr (GATHER) { const unsigned _o0 = (NX) ? vn[h][0] : vc[h][0], _o1 = (NX) ? vn[h][1] : vc[h][1]; PG8_STAGE2(PG8_SA(b, h), (ap), _o0, _o1); } \
;         else { PG8_STAGE2(PG8_SA(b, h), (ap) + (h) * hstepA, voffA[0], voffA[1]); } } while (0)
; #define PG8_LDA(dst, b, h) do { _Pragma("unroll") for (int m = 0; m < 4; ++m) _Pragma("unroll") for (int k = 0; k < 2; ++k) dst[m][k] = *(const LAS bf16x8*)(lds + PG8_SA(b, h) + aoff + m * 2048 + k * 1024); } while (0)
; #define PG8_MMA(ai, bj, At, Bt) do { __builtin_amdgcn_s_setprio(1); _Pragma("unroll") for (int m = 0; m < 4; ++m) _Pragma("unroll") for (int n = 0; n < 2; ++n) _Pragma("unroll") for (int k = 0; k < 2; ++k) \
;         acc[ai][bj][m][n] = __builtin_amdgcn_mfma_f32_16x16x32_bf16(Bt[n][k], At[m][k], acc[ai][bj][m][n], 0, 0, 0); __builtin_amdgcn_s_setprio(0); } while (0)
; #define PG8_WAIT_V(n) asm volatile("s_waitcnt vmcnt(" #n ")" ::: "memory")
; #define PG8_WAIT_L(n) asm volatile("s_waitcnt lgkmcnt(" #n ")" ::: "memory")
; #define PG8_BAR __builtin_amdgcn_s_barrier()
; #define PG8_SCHED __builtin_amdgcn_sched_barrier(0)
; template <class Epi, class Sched, bool GATHER, bool LIGHTSKIP = false>
; __device__ __forceinline__ void gemm_phase(LAS unsigned char* lds, LAS unsigned char* xl, const int lda, const int ldb, const int K, const Sched& S, const Epi& E) {
;     ...
;             PG8_LDA(At, 1, 1); PG8_STAGE_B(1, 0, b3); PG8_STAGE_B(1, 1, b3); PG8_STAGE_A(1, 0, a3, last);
;             PG8_WAIT_V(8); PG8_WAIT_L(0); PG8_BAR; if (!light) { PG8_MMA(1, 0, At, B0); PG8_MMA(1, 1, At, B1); } PG8_BAR; PG8_SCHED;
;         }
	s_add_i32 s46, s62, s5
	v_lshl_add_u64 v[216:217], v[216:217], 0, s[30:31]
	s_mov_b32 m0, s46
	ds_read_b128 v[178:181], v186 offset:49152
	ds_read_b128 v[188:191], v186 offset:50176
	ds_read_b128 v[192:195], v186 offset:51200
	ds_read_b128 v[196:199], v186 offset:52224
	ds_read_b128 v[200:203], v186 offset:53248
	ds_read_b128 v[204:207], v186 offset:54272
	ds_read_b128 v[208:211], v186 offset:55296
	ds_read_b128 v[212:215], v186 offset:56320
	global_load_lds_dwordx4 v[216:217], off
	s_add_i32 m0, s46, 0x2000
	s_add_u32 s44, s44, 0x40080
	v_lshl_add_u64 v[216:217], v[218:219], 0, s[30:31]
	s_addc_u32 s45, s45, 0
	s_add_i32 s46, s63, s5
	global_load_lds_dwordx4 v[216:217], off
	v_lshl_add_u64 v[216:217], s[44:45], 0, v[132:133]
	s_mov_b32 m0, s46
	s_nop 0
	global_load_lds_dwordx4 v[216:217], off
	v_lshl_add_u64 v[216:217], s[44:45], 0, v[136:137]
	s_add_i32 m0, s46, 0x2000
	s_nop 0
	global_load_lds_dwordx4 v[216:217], off
	v_lshl_add_u64 v[216:217], v[220:221], 0, s[30:31]
	s_mov_b32 m0, s48
	s_nop 0
	global_load_lds_dwordx4 v[216:217], off
	v_lshl_add_u64 v[216:217], v[222:223], 0, s[30:31]
	s_mov_b32 m0, s49
	s_nop 0
	global_load_lds_dwordx4 v[216:217], off
	s_waitcnt vmcnt(8)
	s_waitcnt lgkmcnt(0)
	s_barrier
	s_waitcnt lgkmcnt(0)
	v_mfma_f32_16x16x32_bf16 v[62:65], v[146:149], v[178:181], v[62:65]
	v_mfma_f32_16x16x32_bf16 v[58:61], v[154:157], v[178:181], v[58:61]
	v_mfma_f32_16x16x32_bf16 v[46:49], v[146:149], v[192:195], v[46:49]
	v_mfma_f32_16x16x32_bf16 v[42:45], v[154:157], v[192:195], v[42:45]
	v_mfma_f32_16x16x32_bf16 v[30:33], v[146:149], v[200:203], v[30:33]
	v_mfma_f32_16x16x32_bf16 v[26:29], v[154:157], v[200:203], v[26:29]
	v_mfma_f32_16x16x32_bf16 v[14:17], v[146:149], v[208:211], v[14:17]
	v_mfma_f32_16x16x32_bf16 v[10:13], v[154:157], v[208:211], v[10:13]
	v_mfma_f32_16x16x32_bf16 v[62:65], v[150:153], v[188:191], v[62:65]
	v_mfma_f32_16x16x32_bf16 v[58:61], v[158:161], v[188:191], v[58:61]
	v_mfma_f32_16x16x32_bf16 v[46:49], v[150:153], v[196:199], v[46:49]
	v_mfma_f32_16x16x32_bf16 v[42:45], v[158:161], v[196:199], v[42:45]
	v_mfma_f32_16x16x32_bf16 v[30:33], v[150:153], v[204:207], v[30:33]
	v_mfma_f32_16x16x32_bf16 v[26:29], v[158:161], v[204:207], v[26:29]
	v_mfma_f32_16x16x32_bf16 v[14:17], v[150:153], v[212:215], v[14:17]
	v_mfma_f32_16x16x32_bf16 v[10:13], v[158:161], v[212:215], v[10:13]
	v_mfma_f32_16x16x32_bf16 v[54:57], v[162:165], v[178:181], v[54:57]
	v_mfma_f32_16x16x32_bf16 v[50:53], v[170:173], v[178:181], v[50:53]
	v_mfma_f32_16x16x32_bf16 v[38:41], v[162:165], v[192:195], v[38:41]
	v_mfma_f32_16x16x32_bf16 v[34:37], v[170:173], v[192:195], v[34:37]
	v_mfma_f32_16x16x32_bf16 v[22:25], v[162:165], v[200:203], v[22:25]
	v_mfma_f32_16x16x32_bf16 v[18:21], v[170:173], v[200:203], v[18:21]
	v_mfma_f32_16x16x32_bf16 v[6:9], v[162:165], v[208:211], v[6:9]
	v_mfma_f32_16x16x32_bf16 v[2:5], v[170:173], v[208:211], v[2:5]
	v_mfma_f32_16x16x32_bf16 v[54:57], v[166:169], v[188:191], v[54:57]
	v_mfma_f32_16x16x32_bf16 v[50:53], v[174:177], v[188:191], v[50:53]
	v_mfma_f32_16x16x32_bf16 v[38:41], v[166:169], v[196:199], v[38:41]
	v_mfma_f32_16x16x32_bf16 v[34:37], v[174:177], v[196:199], v[34:37]
	v_mfma_f32_16x16x32_bf16 v[22:25], v[166:169], v[204:207], v[22:25]
	v_mfma_f32_16x16x32_bf16 v[18:21], v[174:177], v[204:207], v[18:21]
	v_mfma_f32_16x16x32_bf16 v[6:9], v[166:169], v[212:215], v[6:9]
	v_mfma_f32_16x16x32_bf16 v[2:5], v[174:177], v[212:215], v[2:5]
	s_barrier
	s_add_i32 s61, s61, 2
	s_add_u32 s42, s42, 0x100
	s_addc_u32 s43, s43, 0
	s_add_u32 s59, s59, 0x100
	s_addc_u32 s60, s60, 0
	s_cmp_gt_u32 s61, 13
	s_cbranch_scc0 .LBB0_1027
	s_branch .Lpeel_exit_3
